# speedup vs baseline: 1.0314x; 1.0131x over previous
_Z11prep_kernelPKfS0_PKiPDF16_S3_PfS4_:
	s_lshl_b32 s14, s2, 2
	v_lshrrev_b32_e32 v1, 8, v0
	v_or_b32_e32 v5, s14, v1
	s_movk_i32 s2, 0xff
	v_and_b32_e32 v4, 0xff, v0
	v_cmp_lt_i32_e32 vcc, s2, v5
	s_and_saveexec_b64 s[2:3], vcc
	s_xor_b64 s[2:3], exec, s[2:3]
	s_cbranch_execz .LBB0_5
	v_readfirstlane_b32 s15, v0
	s_and_b32 s16, s15, 0xc0
	s_cmp_eq_u32 s16, 0xc0
	s_cbranch_scc1 .LBB0_7
	s_load_dwordx4 s[8:11], s[0:1], 0x0
	s_load_dwordx4 s[4:7], s[0:1], 0x18
	v_add_u32_e32 v34, 0xffffff00, v5
	v_mov_b32_e32 v35, 0
	v_lshlrev_b64 v[32:33], 11, v[34:35]
	v_lshl_or_b32 v32, v4, 3, v32
	v_lshlrev_b64 v[0:1], 2, v[32:33]
	s_waitcnt lgkmcnt(0)
	s_cmp_lg_u32 s14, 0x100
	s_cbranch_scc1 .Lprep_noflag
	s_cmp_gt_u32 s15, 63
	s_cbranch_scc1 .Lprep_noflag
	s_add_u32 s16, s4, 0x3c08000
	s_addc_u32 s17, s5, 0
	v_lshlrev_b32_e32 v6, 2, v4
	v_mov_b32_e32 v7, 0
	v_mov_b32_e32 v8, s8
	v_mov_b32_e32 v9, s9
	v_mov_b32_e32 v10, s10
	v_mov_b32_e32 v11, s11
	global_store_dword v6, v7, s[16:17]
	global_store_dwordx4 v7, v[8:11], s[16:17] offset:256
.Lprep_noflag:
	v_lshl_add_u64 v[2:3], s[8:9], 0, v[0:1]
	s_mov_b64 s[12:13], 0x1000000
	global_load_dwordx4 v[20:23], v[2:3], off offset:16 nt
	global_load_dwordx4 v[28:31], v[2:3], off nt
	v_lshl_add_u64 v[4:5], v[2:3], 0, s[12:13]
	v_add_co_u32_e32 v2, vcc, 0x1000000, v2
	v_lshl_add_u64 v[0:1], s[10:11], 0, v[0:1]
	s_nop 0
	v_addc_co_u32_e32 v3, vcc, 0, v3, vcc
	global_load_dwordx4 v[24:27], v[2:3], off nt
	global_load_dwordx4 v[16:19], v[4:5], off offset:16 nt
	s_nop 0
	global_load_dwordx4 v[4:7], v[0:1], off offset:16 nt
	global_load_dwordx4 v[8:11], v[0:1], off nt
	s_cmpk_lt_u32 s14, 0x500
	s_cselect_b64 s[8:9], -1, 0
	s_cmpk_gt_u32 s14, 0x4ff
	v_mov_b32_e32 v1, v35
	v_mov_b32_e32 v2, v35
	v_mov_b32_e32 v3, v35
	v_mov_b32_e32 v12, v35
	v_mov_b32_e32 v13, v35
	v_mov_b32_e32 v14, v35
	v_mov_b32_e32 v15, v35
	s_cbranch_scc1 .LBB0_3
	v_lshl_add_u64 v[0:1], v[32:33], 2, s[10:11]
	v_add_co_u32_e32 v36, vcc, 0x1000000, v0
	v_lshl_add_u64 v[34:35], v[0:1], 0, s[12:13]
	s_nop 0
	v_addc_co_u32_e32 v37, vcc, 0, v1, vcc
	global_load_dwordx4 v[0:3], v[36:37], off nt
	global_load_dwordx4 v[12:15], v[34:35], off offset:16 nt
	s_waitcnt vmcnt(1)
	v_mov_b32_e32 v35, v0

	.amdhsa_kernel _Z11prep_kernelPKfS0_PKiPDF16_S3_PfS4_
		.amdhsa_group_segment_fixed_size 0
		.amdhsa_private_segment_fixed_size 0
		.amdhsa_kernarg_size 56
		.amdhsa_user_sgpr_count 2
		.amdhsa_user_sgpr_dispatch_ptr 0
		.amdhsa_user_sgpr_queue_ptr 0
		.amdhsa_user_sgpr_kernarg_segment_ptr 1
		.amdhsa_user_sgpr_dispatch_id 0
		.amdhsa_user_sgpr_kernarg_preload_length 0
		.amdhsa_user_sgpr_kernarg_preload_offset 0
		.amdhsa_user_sgpr_private_segment_size 0
		.amdhsa_uses_dynamic_stack 0
		.amdhsa_enable_private_segment 0
		.amdhsa_system_sgpr_workgroup_id_x 1
		.amdhsa_system_sgpr_workgroup_id_y 0
		.amdhsa_system_sgpr_workgroup_id_z 0
		.amdhsa_system_sgpr_workgroup_info 0
		.amdhsa_system_vgpr_workitem_id 0
		.amdhsa_next_free_vgpr 40
		.amdhsa_next_free_sgpr 18
		.amdhsa_accum_offset 40
		.amdhsa_reserve_vcc 1
		.amdhsa_float_round_mode_32 0
		.amdhsa_float_round_mode_16_64 0
		.amdhsa_float_denorm_mode_32 3
		.amdhsa_float_denorm_mode_16_64 3
		.amdhsa_dx10_clamp 1
		.amdhsa_ieee_mode 1
		.amdhsa_fp16_overflow 0
		.amdhsa_tg_split 0
		.amdhsa_exception_fp_ieee_invalid_op 0
		.amdhsa_exception_fp_denorm_src 0
		.amdhsa_exception_fp_ieee_div_zero 0
		.amdhsa_exception_fp_ieee_overflow 0
		.amdhsa_exception_fp_ieee_underflow 0
		.amdhsa_exception_fp_ieee_inexact 0
		.amdhsa_exception_int_div_zero 0
	.end_amdhsa_kernel

_Z15gemm_qkv_kernelPKDF16_S0_PDF16_S1_S1_PKfS3_S3_S3_S3_S1_PKiPyPj:
	s_load_dwordx8 s[36:43], s[0:1], 0x40
	s_load_dwordx4 s[28:31], s[0:1], 0x60
	s_mov_b64 s[4:5], -1
	s_cmpk_lt_i32 s2, 0xc0
	s_movk_i32 s3, 0xc0
	s_cbranch_scc0 .LBB1_30
	v_lshlrev_b32_e32 v1, 4, v0
	v_and_b32_e32 v2, 32, v0
	v_lshrrev_b32_e32 v4, 1, v0
	v_lshrrev_b32_e32 v5, 5, v0
	v_or_b32_e32 v13, 0x2000, v1
	s_load_dwordx16 s[12:27], s[0:1], 0x0
	v_bfe_u32 v12, v0, 2, 4
	v_bitop3_b32 v10, v1, v2, 48 bitop3:0x6c
	v_and_b32_e32 v4, 24, v4
	v_and_b32_e32 v5, 4, v5
	v_bfe_u32 v6, v0, 2, 2
	v_lshrrev_b32_e32 v1, 7, v13
	s_movk_i32 s0, 0x70
	s_ashr_i32 s33, s2, 31
	v_lshrrev_b32_e32 v3, 2, v0
	v_and_b32_e32 v11, 64, v0
	v_or3_b32 v4, v5, v6, v4
	v_and_or_b32 v1, v1, s0, v12
	s_lshr_b32 s0, s33, 29
	v_readfirstlane_b32 s1, v0
	v_or_b32_e32 v2, v10, v11
	v_and_or_b32 v3, v3, 64, v4
	s_add_i32 s0, s2, s0
	s_lshr_b32 s10, s1, 6
	v_lshl_or_b32 v164, v3, 12, v2
	v_lshrrev_b32_e32 v3, 6, v13
	s_ashr_i32 s4, s0, 3
	s_and_b32 s0, s0, -8
	v_and_or_b32 v3, v3, s3, v4
	s_lshr_b32 s44, s1, 8
	s_lshl_b32 s3, s10, 10
	s_sub_i32 s0, s2, s0
	s_cmp_lt_i32 s0, 0
	s_cselect_b32 s5, 25, 24
	s_mul_i32 s0, s0, s5
	s_add_i32 s0, s0, s4
	s_mul_hi_i32 s4, s0, 0x2aaaaaab
	s_lshr_b32 s5, s4, 31
	s_ashr_i32 s4, s4, 4
	s_add_i32 s4, s4, s5
	s_lshl_b32 s5, s4, 3
	s_mulk_i32 s4, 0x60
	s_sub_i32 s4, s0, s4
	s_bfe_i32 s0, s4, 0x80000
	s_bfe_u32 s0, s0, 0x3000c
	s_add_i32 s6, s4, s0
	s_bfe_i32 s0, s6, 0x80000
	s_and_b32 s6, s6, 0xf8
	s_sub_i32 s4, s4, s6
	s_sext_i32_i16 s0, s0
	s_sext_i32_i8 s4, s4
	s_lshr_b32 s0, s0, 3
	s_add_i32 s4, s5, s4
	s_ashr_i32 s5, s4, 31
	s_bfe_i64 s[8:9], s[0:1], 0x100000
	s_lshl_b64 s[6:7], s[4:5], 20
	s_lshl_b64 s[8:9], s[8:9], 20
	s_waitcnt lgkmcnt(0)
	s_add_u32 s80, s20, 0x408000
	s_addc_u32 s81, s21, 0
	v_and_b32_e32 v241, 63, v0
	v_lshlrev_b32_e32 v241, 2, v241
	s_add_u32 s8, s14, s8
	s_addc_u32 s9, s15, s9
	s_add_i32 s58, s3, 0
	s_add_i32 m0, s58, 0x10000
	v_lshl_or_b32 v168, v3, 12, v2
	global_load_lds_dwordx4 v164, s[8:9]
	s_add_i32 m0, s58, 0x12000
	s_add_u32 s34, s8, 0x20000
	global_load_lds_dwordx4 v168, s[8:9]
	s_addc_u32 s35, s9, 0
	s_add_i32 m0, s58, 0x14000
	v_lshrrev_b32_e32 v5, 3, v0
	global_load_lds_dwordx4 v164, s[34:35]
	s_add_i32 m0, s58, 0x16000
	s_add_u32 s6, s12, s6
	v_and_or_b32 v5, v5, 48, v12
	s_addc_u32 s7, s13, s7
	s_add_i32 s59, s58, 0x2000
	v_lshl_or_b32 v162, v5, 12, v2
	global_load_lds_dwordx4 v168, s[34:35]
	s_mov_b32 m0, s58
	s_add_u32 s34, s6, 0x80000
	v_lshl_or_b32 v166, v1, 12, v2
	global_load_lds_dwordx4 v162, s[6:7]
	s_mov_b32 m0, s59
	s_addc_u32 s35, s7, 0
	s_add_i32 s60, s58, 0x4000
	global_load_lds_dwordx4 v166, s[6:7]
	s_mov_b32 m0, s60
	s_add_i32 s61, s58, 0x6000
	global_load_lds_dwordx4 v162, s[34:35]
	s_mov_b32 m0, s61
	v_mov_b32_e32 v171, 0
	global_load_lds_dwordx4 v166, s[34:35]
	v_mov_b32_e32 v165, v171
	v_mov_b32_e32 v169, v171
	v_mov_b32_e32 v163, v171
	v_mov_b32_e32 v167, v171
	s_cmp_eq_u32 s44, 1
	s_mov_b32 s11, 0
	v_lshl_add_u64 v[8:9], s[8:9], 0, v[164:165]
	v_lshl_add_u64 v[6:7], s[8:9], 0, v[168:169]
	v_lshl_add_u64 v[2:3], s[6:7], 0, v[162:163]
	s_cselect_b64 s[34:35], -1, 0
	s_cmp_lg_u32 s44, 1
	v_lshl_add_u64 v[4:5], s[6:7], 0, v[166:167]
	s_cbranch_scc1 .LBB1_3
	s_barrier

.LBB1_9:
	s_cmp_lg_u32 s56, 18
	s_cbranch_scc1 .Lqkv_noissue
	global_load_dword v240, v241, s[80:81] sc1
.Lqkv_noissue:
	s_cmp_lg_u32 s56, 20
	s_cbranch_scc1 .Lqkv_nopoll
	s_mov_b32 s83, 0
	s_branch .Lqkv_check
.Lqkv_poll:
	global_load_dword v240, v241, s[80:81] sc1
	s_waitcnt vmcnt(0)
.Lqkv_check:
	v_cmp_ne_u32_e32 vcc, 1, v240
	s_cmp_eq_u64 vcc, 0
	s_cbranch_scc1 .Lqkv_nopoll
	s_sleep 16
	s_add_i32 s83, s83, 1
	s_cmpk_lt_u32 s83, 0x190
	s_cbranch_scc1 .Lqkv_poll

.LBB1_30:
	s_and_b64 vcc, exec, s[4:5]
	s_cbranch_vccz .LBB1_41
	s_load_dwordx4 s[44:47], s[0:1], 0x0
	s_load_dwordx2 s[48:49], s[0:1], 0x20
	s_add_i32 s50, s2, 0xffffff40
	v_and_b32_e32 v1, 63, v0
	v_lshrrev_b32_e32 v2, 6, v0
	v_lshlrev_b32_e32 v3, 5, v1
	v_lshl_add_u32 v3, v2, 13, v3
	v_add_u32_e32 v3, 0x1800, v3
	v_lshlrev_b32_e32 v4, 4, v1
	v_lshl_add_u32 v4, v2, 12, v4
	v_add_u32_e32 v4, 0xc00, v4
	s_waitcnt lgkmcnt(0)
	s_add_u32 s48, s48, 0x408000
	s_addc_u32 s49, s49, 0
	s_load_dwordx4 s[52:55], s[48:49], 0x100
	s_lshl_b32 s51, s50, 18
	s_add_u32 s44, s44, s51
	s_addc_u32 s45, s45, 0
	s_mul_i32 s51, s50, 0x30000
	s_add_u32 s46, s46, s51
	s_addc_u32 s47, s47, 0
	s_waitcnt lgkmcnt(0)
	s_lshl_b32 s51, s50, 19
	s_add_u32 s52, s52, s51
	s_addc_u32 s53, s53, 0
	s_mul_i32 s51, s50, 0x60000
	s_add_u32 s54, s54, s51
	s_addc_u32 s55, s55, 0
	global_load_dwordx4 v[16:19], v3, s[52:53] nt
	global_load_dwordx4 v[20:23], v3, s[52:53] offset:16 nt
	s_add_u32 s52, s52, 0x10000
	s_addc_u32 s53, s53, 0
	global_load_dwordx4 v[24:27], v3, s[52:53] nt
	global_load_dwordx4 v[28:31], v3, s[52:53] offset:16 nt
	s_add_u32 s52, s52, 0x10000
	s_addc_u32 s53, s53, 0
	global_load_dwordx4 v[32:35], v3, s[52:53] nt
	global_load_dwordx4 v[36:39], v3, s[52:53] offset:16 nt
	s_add_u32 s52, s52, 0x10000
	s_addc_u32 s53, s53, 0
	global_load_dwordx4 v[40:43], v3, s[52:53] nt
	global_load_dwordx4 v[44:47], v3, s[52:53] offset:16 nt
	s_add_u32 s52, s52, 0x10000
	s_addc_u32 s53, s53, 0
	global_load_dwordx4 v[48:51], v3, s[52:53] nt
	global_load_dwordx4 v[52:55], v3, s[52:53] offset:16 nt
	s_add_u32 s52, s52, 0x10000
	s_addc_u32 s53, s53, 0
	global_load_dwordx4 v[56:59], v3, s[52:53] nt
	global_load_dwordx4 v[60:63], v3, s[52:53] offset:16 nt
	s_add_u32 s52, s52, 0x10000
	s_addc_u32 s53, s53, 0
	global_load_dwordx4 v[64:67], v3, s[52:53] nt
	global_load_dwordx4 v[68:71], v3, s[52:53] offset:16 nt
	s_add_u32 s52, s52, 0x10000
	s_addc_u32 s53, s53, 0
	global_load_dwordx4 v[72:75], v3, s[52:53] nt
	global_load_dwordx4 v[76:79], v3, s[52:53] offset:16 nt
	s_add_u32 s52, s52, 0x10000
	s_addc_u32 s53, s53, 0
	global_load_dwordx4 v[80:83], v3, s[54:55] nt
	global_load_dwordx4 v[84:87], v3, s[54:55] offset:16 nt
	s_add_u32 s54, s54, 0x10000
	s_addc_u32 s55, s55, 0
	global_load_dwordx4 v[88:91], v3, s[54:55] nt
	global_load_dwordx4 v[92:95], v3, s[54:55] offset:16 nt
	s_add_u32 s54, s54, 0x10000
	s_addc_u32 s55, s55, 0
	global_load_dwordx4 v[96:99], v3, s[54:55] nt
	global_load_dwordx4 v[100:103], v3, s[54:55] offset:16 nt
	s_add_u32 s54, s54, 0x10000
	s_addc_u32 s55, s55, 0
	global_load_dwordx4 v[104:107], v3, s[54:55] nt
	global_load_dwordx4 v[108:111], v3, s[54:55] offset:16 nt
	s_add_u32 s54, s54, 0x10000
	s_addc_u32 s55, s55, 0
	global_load_dwordx4 v[112:115], v3, s[54:55] nt
	global_load_dwordx4 v[116:119], v3, s[54:55] offset:16 nt
	s_add_u32 s54, s54, 0x10000
	s_addc_u32 s55, s55, 0
	global_load_dwordx4 v[120:123], v3, s[54:55] nt
	global_load_dwordx4 v[124:127], v3, s[54:55] offset:16 nt
	s_add_u32 s54, s54, 0x10000
	s_addc_u32 s55, s55, 0
	s_waitcnt vmcnt(26)
	v_cvt_pk_f16_f32 v16, v16, v17
	v_cvt_pk_f16_f32 v17, v18, v19
	v_cvt_pk_f16_f32 v18, v20, v21
	v_cvt_pk_f16_f32 v19, v22, v23
	global_store_dwordx4 v4, v[16:19], s[44:45] sc1
	s_add_u32 s44, s44, 0x8000
	s_addc_u32 s45, s45, 0
	s_waitcnt vmcnt(25)
	v_cvt_pk_f16_f32 v24, v24, v25
	v_cvt_pk_f16_f32 v25, v26, v27
	v_cvt_pk_f16_f32 v26, v28, v29
	v_cvt_pk_f16_f32 v27, v30, v31
	global_store_dwordx4 v4, v[24:27], s[44:45] sc1
	s_add_u32 s44, s44, 0x8000
	s_addc_u32 s45, s45, 0
	s_waitcnt vmcnt(24)
	v_cvt_pk_f16_f32 v32, v32, v33
	v_cvt_pk_f16_f32 v33, v34, v35
	v_cvt_pk_f16_f32 v34, v36, v37
	v_cvt_pk_f16_f32 v35, v38, v39
	global_store_dwordx4 v4, v[32:35], s[44:45] sc1
	s_add_u32 s44, s44, 0x8000
	s_addc_u32 s45, s45, 0
	s_waitcnt vmcnt(23)
	v_cvt_pk_f16_f32 v40, v40, v41
	v_cvt_pk_f16_f32 v41, v42, v43
	v_cvt_pk_f16_f32 v42, v44, v45
	v_cvt_pk_f16_f32 v43, v46, v47
	global_store_dwordx4 v4, v[40:43], s[44:45] sc1
	s_add_u32 s44, s44, 0x8000
	s_addc_u32 s45, s45, 0
	s_waitcnt vmcnt(22)
	v_cvt_pk_f16_f32 v48, v48, v49
	v_cvt_pk_f16_f32 v49, v50, v51
	v_cvt_pk_f16_f32 v50, v52, v53
	v_cvt_pk_f16_f32 v51, v54, v55
	global_store_dwordx4 v4, v[48:51], s[44:45] sc1
	s_add_u32 s44, s44, 0x8000
	s_addc_u32 s45, s45, 0
	s_waitcnt vmcnt(21)
	v_cvt_pk_f16_f32 v56, v56, v57
	v_cvt_pk_f16_f32 v57, v58, v59
	v_cvt_pk_f16_f32 v58, v60, v61
	v_cvt_pk_f16_f32 v59, v62, v63
	global_store_dwordx4 v4, v[56:59], s[44:45] sc1
	s_add_u32 s44, s44, 0x8000
	s_addc_u32 s45, s45, 0
	s_waitcnt vmcnt(20)
	v_cvt_pk_f16_f32 v64, v64, v65
	v_cvt_pk_f16_f32 v65, v66, v67
	v_cvt_pk_f16_f32 v66, v68, v69
	v_cvt_pk_f16_f32 v67, v70, v71
	global_store_dwordx4 v4, v[64:67], s[44:45] sc1
	s_add_u32 s44, s44, 0x8000
	s_addc_u32 s45, s45, 0
	s_waitcnt vmcnt(19)
	v_cvt_pk_f16_f32 v72, v72, v73
	v_cvt_pk_f16_f32 v73, v74, v75
	v_cvt_pk_f16_f32 v74, v76, v77
	v_cvt_pk_f16_f32 v75, v78, v79
	global_store_dwordx4 v4, v[72:75], s[44:45] sc1
	s_add_u32 s44, s44, 0x8000
	s_addc_u32 s45, s45, 0
	s_waitcnt vmcnt(18)
	v_cvt_pk_f16_f32 v80, v80, v81
	v_cvt_pk_f16_f32 v81, v82, v83
	v_cvt_pk_f16_f32 v82, v84, v85
	v_cvt_pk_f16_f32 v83, v86, v87
	global_store_dwordx4 v4, v[80:83], s[46:47] sc1
	s_add_u32 s46, s46, 0x8000
	s_addc_u32 s47, s47, 0
	s_waitcnt vmcnt(17)
	v_cvt_pk_f16_f32 v88, v88, v89
	v_cvt_pk_f16_f32 v89, v90, v91
	v_cvt_pk_f16_f32 v90, v92, v93
	v_cvt_pk_f16_f32 v91, v94, v95
	global_store_dwordx4 v4, v[88:91], s[46:47] sc1
	s_add_u32 s46, s46, 0x8000
	s_addc_u32 s47, s47, 0
	s_waitcnt vmcnt(16)
	v_cvt_pk_f16_f32 v96, v96, v97
	v_cvt_pk_f16_f32 v97, v98, v99
	v_cvt_pk_f16_f32 v98, v100, v101
	v_cvt_pk_f16_f32 v99, v102, v103
	global_store_dwordx4 v4, v[96:99], s[46:47] sc1
	s_add_u32 s46, s46, 0x8000
	s_addc_u32 s47, s47, 0
	s_waitcnt vmcnt(15)
	v_cvt_pk_f16_f32 v104, v104, v105
	v_cvt_pk_f16_f32 v105, v106, v107
	v_cvt_pk_f16_f32 v106, v108, v109
	v_cvt_pk_f16_f32 v107, v110, v111
	global_store_dwordx4 v4, v[104:107], s[46:47] sc1
	s_add_u32 s46, s46, 0x8000
	s_addc_u32 s47, s47, 0
	s_waitcnt vmcnt(14)
	v_cvt_pk_f16_f32 v112, v112, v113
	v_cvt_pk_f16_f32 v113, v114, v115
	v_cvt_pk_f16_f32 v114, v116, v117
	v_cvt_pk_f16_f32 v115, v118, v119
	global_store_dwordx4 v4, v[112:115], s[46:47] sc1
	s_add_u32 s46, s46, 0x8000
	s_addc_u32 s47, s47, 0
	s_waitcnt vmcnt(13)
	v_cvt_pk_f16_f32 v120, v120, v121
	v_cvt_pk_f16_f32 v121, v122, v123
	v_cvt_pk_f16_f32 v122, v124, v125
	v_cvt_pk_f16_f32 v123, v126, v127
	global_store_dwordx4 v4, v[120:123], s[46:47] sc1
	s_add_u32 s46, s46, 0x8000
	s_addc_u32 s47, s47, 0
	s_waitcnt vmcnt(0)
	s_barrier
	v_cmp_eq_u32_e32 vcc, 0, v0
	s_and_saveexec_b64 s[56:57], vcc
	v_mov_b32_e32 v5, 1
	v_mov_b32_e32 v6, s50
	v_lshlrev_b32_e32 v6, 2, v6
	global_store_dword v6, v5, s[48:49] sc1
	s_mov_b64 exec, s[56:57]
	s_add_i32 s24, s2, 0xffffff40
	s_lshl_b32 s20, s24, 4
	s_lshl_b32 s0, s24, 5
	s_ashr_i32 s21, s20, 31
	s_and_b32 s25, s0, 0xffffffc0
	s_lshl_b64 s[20:21], s[20:21], 2
	v_lshrrev_b32_e32 v6, 6, v0
	s_waitcnt lgkmcnt(0)
	s_add_u32 s26, s30, s20
	s_addc_u32 s27, s31, s21
	v_lshl_or_b32 v2, v6, 3, s25
	s_and_b32 s25, s2, 1
	s_lshl_b32 s2, s25, 7
	s_add_u32 s20, s28, s2
	v_and_b32_e32 v7, 63, v0
	s_mov_b32 s3, 0
	s_addc_u32 s21, s29, 0
	s_bfe_u32 s2, s24, 0x1a0001
	v_add_u32_e32 v2, v2, v7
	v_mov_b32_e32 v3, 0
	s_lshl_b64 s[2:3], s[2:3], 19
	v_lshl_add_u32 v1, v6, 2, 0
	v_lshlrev_b64 v[4:5], 8, v[2:3]
	v_lshl_or_b32 v2, v6, 16, s2
	s_lshl_b32 s2, s25, 12
	v_lshlrev_b32_e32 v6, 2, v7
	v_cmp_gt_u32_e64 s[0:1], 8, v7
	v_cmp_eq_u32_e64 s[22:23], 0, v7
	v_cmp_eq_u32_e64 s[6:7], 1, v7
	v_cmp_eq_u32_e64 s[8:9], 2, v7
	v_cmp_eq_u32_e64 s[10:11], 3, v7
	v_cmp_eq_u32_e64 s[12:13], 4, v7
	v_cmp_eq_u32_e64 s[14:15], 5, v7
	v_cmp_eq_u32_e64 s[16:17], 6, v7
	v_cmp_eq_u32_e64 s[18:19], 7, v7
	v_or3_b32 v6, v2, s2, v6
	v_mov_b32_e32 v7, s3
	v_cmp_eq_u32_e64 s[4:5], 0, v0
	v_lshl_add_u64 v[4:5], s[20:21], 0, v[4:5]
	v_lshl_add_u64 v[6:7], s[42:43], 0, v[6:7]
	s_mov_b64 s[28:29], 0
	s_lshr_b32 s58, s24, 1
	s_lshl_b32 s58, s58, 19
	s_add_u32 s60, s42, s58
	s_addc_u32 s61, s43, 0
	s_add_u32 s62, s60, 0x2000
	s_addc_u32 s63, s61, 0
	s_add_u32 s64, s62, 0x2000
	s_addc_u32 s65, s63, 0
	s_add_u32 s66, s64, 0x2000
	s_addc_u32 s67, s65, 0
	s_add_u32 s68, s66, 0x2000
	s_addc_u32 s69, s67, 0
	s_add_u32 s70, s68, 0x2000
	s_addc_u32 s71, s69, 0
	s_add_u32 s72, s70, 0x2000
	s_addc_u32 s73, s71, 0
	s_add_u32 s74, s72, 0x2000
	s_addc_u32 s75, s73, 0
	v_lshrrev_b32_e32 v96, 6, v0
	v_lshlrev_b32_e32 v96, 16, v96
	v_and_b32_e32 v97, 63, v0
	v_lshl_add_u32 v96, v97, 2, v96
	s_and_b32 s59, s24, 1
	s_lshl_b32 s59, s59, 12
	v_add_u32_e32 v96, s59, v96
	global_load_dword v100, v96, s[60:61] offset:0 nt
	global_load_dword v101, v96, s[62:63] offset:0 nt
	global_load_dword v102, v96, s[64:65] offset:0 nt
	global_load_dword v103, v96, s[66:67] offset:0 nt
	global_load_dword v104, v96, s[68:69] offset:0 nt
	global_load_dword v105, v96, s[70:71] offset:0 nt
	global_load_dword v106, v96, s[72:73] offset:0 nt
	global_load_dword v107, v96, s[74:75] offset:0 nt
	global_load_dword v108, v96, s[60:61] offset:256 nt
	global_load_dword v109, v96, s[62:63] offset:256 nt
	global_load_dword v110, v96, s[64:65] offset:256 nt
	global_load_dword v111, v96, s[66:67] offset:256 nt
	global_load_dword v112, v96, s[68:69] offset:256 nt
	global_load_dword v113, v96, s[70:71] offset:256 nt
	global_load_dword v114, v96, s[72:73] offset:256 nt
	global_load_dword v115, v96, s[74:75] offset:256 nt
	global_load_dword v116, v96, s[60:61] offset:512 nt
	global_load_dword v117, v96, s[62:63] offset:512 nt
	global_load_dword v118, v96, s[64:65] offset:512 nt
	global_load_dword v119, v96, s[66:67] offset:512 nt
	global_load_dword v120, v96, s[68:69] offset:512 nt
	global_load_dword v121, v96, s[70:71] offset:512 nt
	global_load_dword v122, v96, s[72:73] offset:512 nt
	global_load_dword v123, v96, s[74:75] offset:512 nt
	global_load_dword v124, v96, s[60:61] offset:768 nt
	global_load_dword v125, v96, s[62:63] offset:768 nt
	global_load_dword v126, v96, s[64:65] offset:768 nt
	global_load_dword v127, v96, s[66:67] offset:768 nt
	global_load_dword v128, v96, s[68:69] offset:768 nt
	global_load_dword v129, v96, s[70:71] offset:768 nt
	global_load_dword v130, v96, s[72:73] offset:768 nt
	global_load_dword v131, v96, s[74:75] offset:768 nt
	global_load_dword v132, v96, s[60:61] offset:1024 nt
	global_load_dword v133, v96, s[62:63] offset:1024 nt
	global_load_dword v134, v96, s[64:65] offset:1024 nt
	global_load_dword v135, v96, s[66:67] offset:1024 nt
	global_load_dword v136, v96, s[68:69] offset:1024 nt
	global_load_dword v137, v96, s[70:71] offset:1024 nt
	global_load_dword v138, v96, s[72:73] offset:1024 nt
	global_load_dword v139, v96, s[74:75] offset:1024 nt
	global_load_dword v140, v96, s[60:61] offset:1280 nt
	global_load_dword v141, v96, s[62:63] offset:1280 nt
	global_load_dword v142, v96, s[64:65] offset:1280 nt
	global_load_dword v143, v96, s[66:67] offset:1280 nt
	global_load_dword v144, v96, s[68:69] offset:1280 nt
	global_load_dword v145, v96, s[70:71] offset:1280 nt
	global_load_dword v146, v96, s[72:73] offset:1280 nt
	global_load_dword v147, v96, s[74:75] offset:1280 nt
	global_load_dword v148, v96, s[60:61] offset:1536 nt
	global_load_dword v149, v96, s[62:63] offset:1536 nt
	global_load_dword v150, v96, s[64:65] offset:1536 nt
	global_load_dword v151, v96, s[66:67] offset:1536 nt
	global_load_dword v152, v96, s[68:69] offset:1536 nt
	global_load_dword v153, v96, s[70:71] offset:1536 nt
	global_load_dword v154, v96, s[72:73] offset:1536 nt
	global_load_dword v155, v96, s[74:75] offset:1536 nt
	s_waitcnt vmcnt(48)
	v_cmp_ne_u32_e32 vcc, 0, v100
	s_nop 1
	v_mov_b32_e32 v2, vcc_lo
	v_mov_b32_e32 v9, vcc_hi
	v_cmp_ne_u32_e32 vcc, 0, v101
	v_cndmask_b32_e64 v2, 0, v2, s[22:23]
	v_cndmask_b32_e64 v9, 0, v9, s[22:23]
	v_mov_b32_e32 v11, vcc_hi
	v_mov_b32_e32 v14, vcc_lo
	v_cndmask_b32_e64 v9, v9, v11, s[6:7]
	v_cndmask_b32_e64 v2, v2, v14, s[6:7]
	v_cmp_ne_u32_e32 vcc, 0, v102
	s_nop 1
	v_mov_b32_e32 v11, vcc_lo
	v_mov_b32_e32 v14, vcc_hi
	v_cmp_ne_u32_e32 vcc, 0, v103
	v_cndmask_b32_e64 v2, v2, v11, s[8:9]
	v_cndmask_b32_e64 v9, v9, v14, s[8:9]
	v_mov_b32_e32 v11, vcc_hi
	v_mov_b32_e32 v14, vcc_lo
	v_cmp_ne_u32_e32 vcc, 0, v104
	v_cndmask_b32_e64 v9, v9, v11, s[10:11]
	v_cndmask_b32_e64 v2, v2, v14, s[10:11]
	v_mov_b32_e32 v11, vcc_lo
	v_mov_b32_e32 v12, vcc_hi
	v_cmp_ne_u32_e32 vcc, 0, v105
	v_cndmask_b32_e64 v2, v2, v11, s[12:13]
	v_cndmask_b32_e64 v9, v9, v12, s[12:13]
	v_mov_b32_e32 v11, vcc_hi
	v_mov_b32_e32 v12, vcc_lo
	v_cndmask_b32_e64 v9, v9, v11, s[14:15]
	v_cndmask_b32_e64 v2, v2, v12, s[14:15]
	v_cmp_ne_u32_e32 vcc, 0, v106
	s_nop 1
	v_mov_b32_e32 v10, vcc_lo
	v_mov_b32_e32 v11, vcc_hi
	v_cmp_ne_u32_e32 vcc, 0, v107
	v_cndmask_b32_e64 v2, v2, v10, s[16:17]
	v_cndmask_b32_e64 v8, v9, v11, s[16:17]
	v_mov_b32_e32 v9, vcc_hi
	v_mov_b32_e32 v10, vcc_lo
	v_cndmask_b32_e64 v9, v8, v9, s[18:19]
	v_cndmask_b32_e64 v8, v2, v10, s[18:19]
	s_and_saveexec_b64 s[2:3], s[0:1]
	s_cbranch_execz .Lmk35_0
	global_store_dwordx2 v[4:5], v[8:9], off

.Lmk32_0:
	s_or_b64 exec, exec, s[2:3]
	v_lshl_add_u64 v[4:5], v[4:5], 0, 8
	s_barrier
	global_load_dword v156, v96, s[60:61] offset:1792 nt
	global_load_dword v157, v96, s[62:63] offset:1792 nt
	global_load_dword v158, v96, s[64:65] offset:1792 nt
	global_load_dword v159, v96, s[66:67] offset:1792 nt
	global_load_dword v160, v96, s[68:69] offset:1792 nt
	global_load_dword v161, v96, s[70:71] offset:1792 nt
	global_load_dword v162, v96, s[72:73] offset:1792 nt
	global_load_dword v163, v96, s[74:75] offset:1792 nt
	s_waitcnt vmcnt(49)
	v_cmp_ne_u32_e32 vcc, 0, v108
	s_nop 1
	v_mov_b32_e32 v2, vcc_lo
	v_mov_b32_e32 v9, vcc_hi
	v_cmp_ne_u32_e32 vcc, 0, v109
	v_cndmask_b32_e64 v2, 0, v2, s[22:23]
	v_cndmask_b32_e64 v9, 0, v9, s[22:23]
	v_mov_b32_e32 v11, vcc_hi
	v_mov_b32_e32 v14, vcc_lo
	v_cndmask_b32_e64 v9, v9, v11, s[6:7]
	v_cndmask_b32_e64 v2, v2, v14, s[6:7]
	v_cmp_ne_u32_e32 vcc, 0, v110
	s_nop 1
	v_mov_b32_e32 v11, vcc_lo
	v_mov_b32_e32 v14, vcc_hi
	v_cmp_ne_u32_e32 vcc, 0, v111
	v_cndmask_b32_e64 v2, v2, v11, s[8:9]
	v_cndmask_b32_e64 v9, v9, v14, s[8:9]
	v_mov_b32_e32 v11, vcc_hi
	v_mov_b32_e32 v14, vcc_lo
	v_cmp_ne_u32_e32 vcc, 0, v112
	v_cndmask_b32_e64 v9, v9, v11, s[10:11]
	v_cndmask_b32_e64 v2, v2, v14, s[10:11]
	v_mov_b32_e32 v11, vcc_lo
	v_mov_b32_e32 v12, vcc_hi
	v_cmp_ne_u32_e32 vcc, 0, v113
	v_cndmask_b32_e64 v2, v2, v11, s[12:13]
	v_cndmask_b32_e64 v9, v9, v12, s[12:13]
	v_mov_b32_e32 v11, vcc_hi
	v_mov_b32_e32 v12, vcc_lo
	v_cndmask_b32_e64 v9, v9, v11, s[14:15]
	v_cndmask_b32_e64 v2, v2, v12, s[14:15]
	v_cmp_ne_u32_e32 vcc, 0, v114
	s_nop 1
	v_mov_b32_e32 v10, vcc_lo
	v_mov_b32_e32 v11, vcc_hi
	v_cmp_ne_u32_e32 vcc, 0, v115
	v_cndmask_b32_e64 v2, v2, v10, s[16:17]
	v_cndmask_b32_e64 v8, v9, v11, s[16:17]
	v_mov_b32_e32 v9, vcc_hi
	v_mov_b32_e32 v10, vcc_lo
	v_cndmask_b32_e64 v9, v8, v9, s[18:19]
	v_cndmask_b32_e64 v8, v2, v10, s[18:19]
	s_and_saveexec_b64 s[2:3], s[0:1]
	s_cbranch_execz .Lmk35_1
	global_store_dwordx2 v[4:5], v[8:9], off

.Lmk37_1:
	s_or_b64 exec, exec, s[2:3]
	s_waitcnt lgkmcnt(0)
	s_barrier
	s_and_saveexec_b64 s[2:3], s[4:5]
	s_cbranch_execz .Lmk32_1
	ds_read_b128 v[8:11], v3 offset:32
	ds_read_b128 v[12:15], v3
	ds_read_b128 v[16:19], v3 offset:16
	ds_read_b128 v[20:23], v3 offset:48
	s_waitcnt lgkmcnt(3)
	v_or_b32_e32 v2, v9, v8
	s_waitcnt lgkmcnt(2)
	v_or_b32_e32 v8, v13, v12
	v_or_b32_e32 v8, v8, v14
	v_or_b32_e32 v2, v2, v10
	v_or_b32_e32 v8, v8, v15
	v_or_b32_e32 v2, v2, v11
	s_waitcnt lgkmcnt(1)
	v_or_b32_e32 v8, v8, v16
	s_waitcnt lgkmcnt(0)
	v_or_b32_e32 v2, v2, v20
	v_or_b32_e32 v8, v8, v17
	v_or_b32_e32 v2, v2, v21
	v_or_b32_e32 v8, v8, v18
	v_or_b32_e32 v2, v2, v22
	v_or_b32_e32 v8, v8, v19
	v_or_b32_e32 v2, v2, v23
	v_cmp_ne_u32_e32 vcc, 0, v8
	s_nop 1
	v_cndmask_b32_e64 v8, 0, 1, vcc
	v_cmp_eq_u32_e32 vcc, 0, v2
	s_nop 1
	v_cndmask_b32_e64 v2, 2, 0, vcc
	v_or_b32_e32 v2, v2, v8
	global_store_dword v3, v2, s[26:27] offset:4
.Lmk32_1:
	s_or_b64 exec, exec, s[2:3]
	v_lshl_add_u64 v[4:5], v[4:5], 0, 8
	s_barrier
	global_load_dword v164, v96, s[60:61] offset:2048 nt
	global_load_dword v165, v96, s[62:63] offset:2048 nt
	global_load_dword v166, v96, s[64:65] offset:2048 nt
	global_load_dword v167, v96, s[66:67] offset:2048 nt
	global_load_dword v168, v96, s[68:69] offset:2048 nt
	global_load_dword v169, v96, s[70:71] offset:2048 nt
	global_load_dword v170, v96, s[72:73] offset:2048 nt
	global_load_dword v171, v96, s[74:75] offset:2048 nt
	s_waitcnt vmcnt(50)
	v_cmp_ne_u32_e32 vcc, 0, v116
	s_nop 1
	v_mov_b32_e32 v2, vcc_lo
	v_mov_b32_e32 v9, vcc_hi
	v_cmp_ne_u32_e32 vcc, 0, v117
	v_cndmask_b32_e64 v2, 0, v2, s[22:23]
	v_cndmask_b32_e64 v9, 0, v9, s[22:23]
	v_mov_b32_e32 v11, vcc_hi
	v_mov_b32_e32 v14, vcc_lo
	v_cndmask_b32_e64 v9, v9, v11, s[6:7]
	v_cndmask_b32_e64 v2, v2, v14, s[6:7]
	v_cmp_ne_u32_e32 vcc, 0, v118
	s_nop 1
	v_mov_b32_e32 v11, vcc_lo
	v_mov_b32_e32 v14, vcc_hi
	v_cmp_ne_u32_e32 vcc, 0, v119
	v_cndmask_b32_e64 v2, v2, v11, s[8:9]
	v_cndmask_b32_e64 v9, v9, v14, s[8:9]
	v_mov_b32_e32 v11, vcc_hi
	v_mov_b32_e32 v14, vcc_lo
	v_cmp_ne_u32_e32 vcc, 0, v120
	v_cndmask_b32_e64 v9, v9, v11, s[10:11]
	v_cndmask_b32_e64 v2, v2, v14, s[10:11]
	v_mov_b32_e32 v11, vcc_lo
	v_mov_b32_e32 v12, vcc_hi
	v_cmp_ne_u32_e32 vcc, 0, v121
	v_cndmask_b32_e64 v2, v2, v11, s[12:13]
	v_cndmask_b32_e64 v9, v9, v12, s[12:13]
	v_mov_b32_e32 v11, vcc_hi
	v_mov_b32_e32 v12, vcc_lo
	v_cndmask_b32_e64 v9, v9, v11, s[14:15]
	v_cndmask_b32_e64 v2, v2, v12, s[14:15]
	v_cmp_ne_u32_e32 vcc, 0, v122
	s_nop 1
	v_mov_b32_e32 v10, vcc_lo
	v_mov_b32_e32 v11, vcc_hi
	v_cmp_ne_u32_e32 vcc, 0, v123
	v_cndmask_b32_e64 v2, v2, v10, s[16:17]
	v_cndmask_b32_e64 v8, v9, v11, s[16:17]
	v_mov_b32_e32 v9, vcc_hi
	v_mov_b32_e32 v10, vcc_lo
	v_cndmask_b32_e64 v9, v8, v9, s[18:19]
	v_cndmask_b32_e64 v8, v2, v10, s[18:19]
	s_and_saveexec_b64 s[2:3], s[0:1]
	s_cbranch_execz .Lmk35_2
	global_store_dwordx2 v[4:5], v[8:9], off

.Lmk37_2:
	s_or_b64 exec, exec, s[2:3]
	s_waitcnt lgkmcnt(0)
	s_barrier
	s_and_saveexec_b64 s[2:3], s[4:5]
	s_cbranch_execz .Lmk32_2
	ds_read_b128 v[8:11], v3 offset:32
	ds_read_b128 v[12:15], v3
	ds_read_b128 v[16:19], v3 offset:16
	ds_read_b128 v[20:23], v3 offset:48
	s_waitcnt lgkmcnt(3)
	v_or_b32_e32 v2, v9, v8
	s_waitcnt lgkmcnt(2)
	v_or_b32_e32 v8, v13, v12
	v_or_b32_e32 v8, v8, v14
	v_or_b32_e32 v2, v2, v10
	v_or_b32_e32 v8, v8, v15
	v_or_b32_e32 v2, v2, v11
	s_waitcnt lgkmcnt(1)
	v_or_b32_e32 v8, v8, v16
	s_waitcnt lgkmcnt(0)
	v_or_b32_e32 v2, v2, v20
	v_or_b32_e32 v8, v8, v17
	v_or_b32_e32 v2, v2, v21
	v_or_b32_e32 v8, v8, v18
	v_or_b32_e32 v2, v2, v22
	v_or_b32_e32 v8, v8, v19
	v_or_b32_e32 v2, v2, v23
	v_cmp_ne_u32_e32 vcc, 0, v8
	s_nop 1
	v_cndmask_b32_e64 v8, 0, 1, vcc
	v_cmp_eq_u32_e32 vcc, 0, v2
	s_nop 1
	v_cndmask_b32_e64 v2, 2, 0, vcc
	v_or_b32_e32 v2, v2, v8
	global_store_dword v3, v2, s[26:27] offset:8
.Lmk32_2:
	s_or_b64 exec, exec, s[2:3]
	v_lshl_add_u64 v[4:5], v[4:5], 0, 8
	s_barrier
	global_load_dword v172, v96, s[60:61] offset:2304 nt
	global_load_dword v173, v96, s[62:63] offset:2304 nt
	global_load_dword v174, v96, s[64:65] offset:2304 nt
	global_load_dword v175, v96, s[66:67] offset:2304 nt
	global_load_dword v176, v96, s[68:69] offset:2304 nt
	global_load_dword v177, v96, s[70:71] offset:2304 nt
	global_load_dword v178, v96, s[72:73] offset:2304 nt
	global_load_dword v179, v96, s[74:75] offset:2304 nt
	s_waitcnt vmcnt(51)
	v_cmp_ne_u32_e32 vcc, 0, v124
	s_nop 1
	v_mov_b32_e32 v2, vcc_lo
	v_mov_b32_e32 v9, vcc_hi
	v_cmp_ne_u32_e32 vcc, 0, v125
	v_cndmask_b32_e64 v2, 0, v2, s[22:23]
	v_cndmask_b32_e64 v9, 0, v9, s[22:23]
	v_mov_b32_e32 v11, vcc_hi
	v_mov_b32_e32 v14, vcc_lo
	v_cndmask_b32_e64 v9, v9, v11, s[6:7]
	v_cndmask_b32_e64 v2, v2, v14, s[6:7]
	v_cmp_ne_u32_e32 vcc, 0, v126
	s_nop 1
	v_mov_b32_e32 v11, vcc_lo
	v_mov_b32_e32 v14, vcc_hi
	v_cmp_ne_u32_e32 vcc, 0, v127
	v_cndmask_b32_e64 v2, v2, v11, s[8:9]
	v_cndmask_b32_e64 v9, v9, v14, s[8:9]
	v_mov_b32_e32 v11, vcc_hi
	v_mov_b32_e32 v14, vcc_lo
	v_cmp_ne_u32_e32 vcc, 0, v128
	v_cndmask_b32_e64 v9, v9, v11, s[10:11]
	v_cndmask_b32_e64 v2, v2, v14, s[10:11]
	v_mov_b32_e32 v11, vcc_lo
	v_mov_b32_e32 v12, vcc_hi
	v_cmp_ne_u32_e32 vcc, 0, v129
	v_cndmask_b32_e64 v2, v2, v11, s[12:13]
	v_cndmask_b32_e64 v9, v9, v12, s[12:13]
	v_mov_b32_e32 v11, vcc_hi
	v_mov_b32_e32 v12, vcc_lo
	v_cndmask_b32_e64 v9, v9, v11, s[14:15]
	v_cndmask_b32_e64 v2, v2, v12, s[14:15]
	v_cmp_ne_u32_e32 vcc, 0, v130
	s_nop 1
	v_mov_b32_e32 v10, vcc_lo
	v_mov_b32_e32 v11, vcc_hi
	v_cmp_ne_u32_e32 vcc, 0, v131
	v_cndmask_b32_e64 v2, v2, v10, s[16:17]
	v_cndmask_b32_e64 v8, v9, v11, s[16:17]
	v_mov_b32_e32 v9, vcc_hi
	v_mov_b32_e32 v10, vcc_lo
	v_cndmask_b32_e64 v9, v8, v9, s[18:19]
	v_cndmask_b32_e64 v8, v2, v10, s[18:19]
	s_and_saveexec_b64 s[2:3], s[0:1]
	s_cbranch_execz .Lmk35_3
	global_store_dwordx2 v[4:5], v[8:9], off

.Lmk37_3:
	s_or_b64 exec, exec, s[2:3]
	s_waitcnt lgkmcnt(0)
	s_barrier
	s_and_saveexec_b64 s[2:3], s[4:5]
	s_cbranch_execz .Lmk32_3
	ds_read_b128 v[8:11], v3 offset:32
	ds_read_b128 v[12:15], v3
	ds_read_b128 v[16:19], v3 offset:16
	ds_read_b128 v[20:23], v3 offset:48
	s_waitcnt lgkmcnt(3)
	v_or_b32_e32 v2, v9, v8
	s_waitcnt lgkmcnt(2)
	v_or_b32_e32 v8, v13, v12
	v_or_b32_e32 v8, v8, v14
	v_or_b32_e32 v2, v2, v10
	v_or_b32_e32 v8, v8, v15
	v_or_b32_e32 v2, v2, v11
	s_waitcnt lgkmcnt(1)
	v_or_b32_e32 v8, v8, v16
	s_waitcnt lgkmcnt(0)
	v_or_b32_e32 v2, v2, v20
	v_or_b32_e32 v8, v8, v17
	v_or_b32_e32 v2, v2, v21
	v_or_b32_e32 v8, v8, v18
	v_or_b32_e32 v2, v2, v22
	v_or_b32_e32 v8, v8, v19
	v_or_b32_e32 v2, v2, v23
	v_cmp_ne_u32_e32 vcc, 0, v8
	s_nop 1
	v_cndmask_b32_e64 v8, 0, 1, vcc
	v_cmp_eq_u32_e32 vcc, 0, v2
	s_nop 1
	v_cndmask_b32_e64 v2, 2, 0, vcc
	v_or_b32_e32 v2, v2, v8
	global_store_dword v3, v2, s[26:27] offset:12
.Lmk32_3:
	s_or_b64 exec, exec, s[2:3]
	v_lshl_add_u64 v[4:5], v[4:5], 0, 8
	s_barrier
	global_load_dword v180, v96, s[60:61] offset:2560 nt
	global_load_dword v181, v96, s[62:63] offset:2560 nt
	global_load_dword v182, v96, s[64:65] offset:2560 nt
	global_load_dword v183, v96, s[66:67] offset:2560 nt
	global_load_dword v184, v96, s[68:69] offset:2560 nt
	global_load_dword v185, v96, s[70:71] offset:2560 nt
	global_load_dword v186, v96, s[72:73] offset:2560 nt
	global_load_dword v187, v96, s[74:75] offset:2560 nt
	s_waitcnt vmcnt(52)
	v_cmp_ne_u32_e32 vcc, 0, v132
	s_nop 1
	v_mov_b32_e32 v2, vcc_lo
	v_mov_b32_e32 v9, vcc_hi
	v_cmp_ne_u32_e32 vcc, 0, v133
	v_cndmask_b32_e64 v2, 0, v2, s[22:23]
	v_cndmask_b32_e64 v9, 0, v9, s[22:23]
	v_mov_b32_e32 v11, vcc_hi
	v_mov_b32_e32 v14, vcc_lo
	v_cndmask_b32_e64 v9, v9, v11, s[6:7]
	v_cndmask_b32_e64 v2, v2, v14, s[6:7]
	v_cmp_ne_u32_e32 vcc, 0, v134
	s_nop 1
	v_mov_b32_e32 v11, vcc_lo
	v_mov_b32_e32 v14, vcc_hi
	v_cmp_ne_u32_e32 vcc, 0, v135
	v_cndmask_b32_e64 v2, v2, v11, s[8:9]
	v_cndmask_b32_e64 v9, v9, v14, s[8:9]
	v_mov_b32_e32 v11, vcc_hi
	v_mov_b32_e32 v14, vcc_lo
	v_cmp_ne_u32_e32 vcc, 0, v136
	v_cndmask_b32_e64 v9, v9, v11, s[10:11]
	v_cndmask_b32_e64 v2, v2, v14, s[10:11]
	v_mov_b32_e32 v11, vcc_lo
	v_mov_b32_e32 v12, vcc_hi
	v_cmp_ne_u32_e32 vcc, 0, v137
	v_cndmask_b32_e64 v2, v2, v11, s[12:13]
	v_cndmask_b32_e64 v9, v9, v12, s[12:13]
	v_mov_b32_e32 v11, vcc_hi
	v_mov_b32_e32 v12, vcc_lo
	v_cndmask_b32_e64 v9, v9, v11, s[14:15]
	v_cndmask_b32_e64 v2, v2, v12, s[14:15]
	v_cmp_ne_u32_e32 vcc, 0, v138
	s_nop 1
	v_mov_b32_e32 v10, vcc_lo
	v_mov_b32_e32 v11, vcc_hi
	v_cmp_ne_u32_e32 vcc, 0, v139
	v_cndmask_b32_e64 v2, v2, v10, s[16:17]
	v_cndmask_b32_e64 v8, v9, v11, s[16:17]
	v_mov_b32_e32 v9, vcc_hi
	v_mov_b32_e32 v10, vcc_lo
	v_cndmask_b32_e64 v9, v8, v9, s[18:19]
	v_cndmask_b32_e64 v8, v2, v10, s[18:19]
	s_and_saveexec_b64 s[2:3], s[0:1]
	s_cbranch_execz .Lmk35_4
	global_store_dwordx2 v[4:5], v[8:9], off

.Lmk37_4:
	s_or_b64 exec, exec, s[2:3]
	s_waitcnt lgkmcnt(0)
	s_barrier
	s_and_saveexec_b64 s[2:3], s[4:5]
	s_cbranch_execz .Lmk32_4
	ds_read_b128 v[8:11], v3 offset:32
	ds_read_b128 v[12:15], v3
	ds_read_b128 v[16:19], v3 offset:16
	ds_read_b128 v[20:23], v3 offset:48
	s_waitcnt lgkmcnt(3)
	v_or_b32_e32 v2, v9, v8
	s_waitcnt lgkmcnt(2)
	v_or_b32_e32 v8, v13, v12
	v_or_b32_e32 v8, v8, v14
	v_or_b32_e32 v2, v2, v10
	v_or_b32_e32 v8, v8, v15
	v_or_b32_e32 v2, v2, v11
	s_waitcnt lgkmcnt(1)
	v_or_b32_e32 v8, v8, v16
	s_waitcnt lgkmcnt(0)
	v_or_b32_e32 v2, v2, v20
	v_or_b32_e32 v8, v8, v17
	v_or_b32_e32 v2, v2, v21
	v_or_b32_e32 v8, v8, v18
	v_or_b32_e32 v2, v2, v22
	v_or_b32_e32 v8, v8, v19
	v_or_b32_e32 v2, v2, v23
	v_cmp_ne_u32_e32 vcc, 0, v8
	s_nop 1
	v_cndmask_b32_e64 v8, 0, 1, vcc
	v_cmp_eq_u32_e32 vcc, 0, v2
	s_nop 1
	v_cndmask_b32_e64 v2, 2, 0, vcc
	v_or_b32_e32 v2, v2, v8
	global_store_dword v3, v2, s[26:27] offset:16
.Lmk32_4:
	s_or_b64 exec, exec, s[2:3]
	v_lshl_add_u64 v[4:5], v[4:5], 0, 8
	s_barrier
	global_load_dword v188, v96, s[60:61] offset:2816 nt
	global_load_dword v189, v96, s[62:63] offset:2816 nt
	global_load_dword v190, v96, s[64:65] offset:2816 nt
	global_load_dword v191, v96, s[66:67] offset:2816 nt
	global_load_dword v192, v96, s[68:69] offset:2816 nt
	global_load_dword v193, v96, s[70:71] offset:2816 nt
	global_load_dword v194, v96, s[72:73] offset:2816 nt
	global_load_dword v195, v96, s[74:75] offset:2816 nt
	s_waitcnt vmcnt(53)
	v_cmp_ne_u32_e32 vcc, 0, v140
	s_nop 1
	v_mov_b32_e32 v2, vcc_lo
	v_mov_b32_e32 v9, vcc_hi
	v_cmp_ne_u32_e32 vcc, 0, v141
	v_cndmask_b32_e64 v2, 0, v2, s[22:23]
	v_cndmask_b32_e64 v9, 0, v9, s[22:23]
	v_mov_b32_e32 v11, vcc_hi
	v_mov_b32_e32 v14, vcc_lo
	v_cndmask_b32_e64 v9, v9, v11, s[6:7]
	v_cndmask_b32_e64 v2, v2, v14, s[6:7]
	v_cmp_ne_u32_e32 vcc, 0, v142
	s_nop 1
	v_mov_b32_e32 v11, vcc_lo
	v_mov_b32_e32 v14, vcc_hi
	v_cmp_ne_u32_e32 vcc, 0, v143
	v_cndmask_b32_e64 v2, v2, v11, s[8:9]
	v_cndmask_b32_e64 v9, v9, v14, s[8:9]
	v_mov_b32_e32 v11, vcc_hi
	v_mov_b32_e32 v14, vcc_lo
	v_cmp_ne_u32_e32 vcc, 0, v144
	v_cndmask_b32_e64 v9, v9, v11, s[10:11]
	v_cndmask_b32_e64 v2, v2, v14, s[10:11]
	v_mov_b32_e32 v11, vcc_lo
	v_mov_b32_e32 v12, vcc_hi
	v_cmp_ne_u32_e32 vcc, 0, v145
	v_cndmask_b32_e64 v2, v2, v11, s[12:13]
	v_cndmask_b32_e64 v9, v9, v12, s[12:13]
	v_mov_b32_e32 v11, vcc_hi
	v_mov_b32_e32 v12, vcc_lo
	v_cndmask_b32_e64 v9, v9, v11, s[14:15]
	v_cndmask_b32_e64 v2, v2, v12, s[14:15]
	v_cmp_ne_u32_e32 vcc, 0, v146
	s_nop 1
	v_mov_b32_e32 v10, vcc_lo
	v_mov_b32_e32 v11, vcc_hi
	v_cmp_ne_u32_e32 vcc, 0, v147
	v_cndmask_b32_e64 v2, v2, v10, s[16:17]
	v_cndmask_b32_e64 v8, v9, v11, s[16:17]
	v_mov_b32_e32 v9, vcc_hi
	v_mov_b32_e32 v10, vcc_lo
	v_cndmask_b32_e64 v9, v8, v9, s[18:19]
	v_cndmask_b32_e64 v8, v2, v10, s[18:19]
	s_and_saveexec_b64 s[2:3], s[0:1]
	s_cbranch_execz .Lmk35_5
	global_store_dwordx2 v[4:5], v[8:9], off

.Lmk37_5:
	s_or_b64 exec, exec, s[2:3]
	s_waitcnt lgkmcnt(0)
	s_barrier
	s_and_saveexec_b64 s[2:3], s[4:5]
	s_cbranch_execz .Lmk32_5
	ds_read_b128 v[8:11], v3 offset:32
	ds_read_b128 v[12:15], v3
	ds_read_b128 v[16:19], v3 offset:16
	ds_read_b128 v[20:23], v3 offset:48
	s_waitcnt lgkmcnt(3)
	v_or_b32_e32 v2, v9, v8
	s_waitcnt lgkmcnt(2)
	v_or_b32_e32 v8, v13, v12
	v_or_b32_e32 v8, v8, v14
	v_or_b32_e32 v2, v2, v10
	v_or_b32_e32 v8, v8, v15
	v_or_b32_e32 v2, v2, v11
	s_waitcnt lgkmcnt(1)
	v_or_b32_e32 v8, v8, v16
	s_waitcnt lgkmcnt(0)
	v_or_b32_e32 v2, v2, v20
	v_or_b32_e32 v8, v8, v17
	v_or_b32_e32 v2, v2, v21
	v_or_b32_e32 v8, v8, v18
	v_or_b32_e32 v2, v2, v22
	v_or_b32_e32 v8, v8, v19
	v_or_b32_e32 v2, v2, v23
	v_cmp_ne_u32_e32 vcc, 0, v8
	s_nop 1
	v_cndmask_b32_e64 v8, 0, 1, vcc
	v_cmp_eq_u32_e32 vcc, 0, v2
	s_nop 1
	v_cndmask_b32_e64 v2, 2, 0, vcc
	v_or_b32_e32 v2, v2, v8
	global_store_dword v3, v2, s[26:27] offset:20
.Lmk32_5:
	s_or_b64 exec, exec, s[2:3]
	v_lshl_add_u64 v[4:5], v[4:5], 0, 8
	s_barrier
	global_load_dword v196, v96, s[60:61] offset:3072 nt
	global_load_dword v197, v96, s[62:63] offset:3072 nt
	global_load_dword v198, v96, s[64:65] offset:3072 nt
	global_load_dword v199, v96, s[66:67] offset:3072 nt
	global_load_dword v200, v96, s[68:69] offset:3072 nt
	global_load_dword v201, v96, s[70:71] offset:3072 nt
	global_load_dword v202, v96, s[72:73] offset:3072 nt
	global_load_dword v203, v96, s[74:75] offset:3072 nt
	s_waitcnt vmcnt(54)
	v_cmp_ne_u32_e32 vcc, 0, v148
	s_nop 1
	v_mov_b32_e32 v2, vcc_lo
	v_mov_b32_e32 v9, vcc_hi
	v_cmp_ne_u32_e32 vcc, 0, v149
	v_cndmask_b32_e64 v2, 0, v2, s[22:23]
	v_cndmask_b32_e64 v9, 0, v9, s[22:23]
	v_mov_b32_e32 v11, vcc_hi
	v_mov_b32_e32 v14, vcc_lo
	v_cndmask_b32_e64 v9, v9, v11, s[6:7]
	v_cndmask_b32_e64 v2, v2, v14, s[6:7]
	v_cmp_ne_u32_e32 vcc, 0, v150
	s_nop 1
	v_mov_b32_e32 v11, vcc_lo
	v_mov_b32_e32 v14, vcc_hi
	v_cmp_ne_u32_e32 vcc, 0, v151
	v_cndmask_b32_e64 v2, v2, v11, s[8:9]
	v_cndmask_b32_e64 v9, v9, v14, s[8:9]
	v_mov_b32_e32 v11, vcc_hi
	v_mov_b32_e32 v14, vcc_lo
	v_cmp_ne_u32_e32 vcc, 0, v152
	v_cndmask_b32_e64 v9, v9, v11, s[10:11]
	v_cndmask_b32_e64 v2, v2, v14, s[10:11]
	v_mov_b32_e32 v11, vcc_lo
	v_mov_b32_e32 v12, vcc_hi
	v_cmp_ne_u32_e32 vcc, 0, v153
	v_cndmask_b32_e64 v2, v2, v11, s[12:13]
	v_cndmask_b32_e64 v9, v9, v12, s[12:13]
	v_mov_b32_e32 v11, vcc_hi
	v_mov_b32_e32 v12, vcc_lo
	v_cndmask_b32_e64 v9, v9, v11, s[14:15]
	v_cndmask_b32_e64 v2, v2, v12, s[14:15]
	v_cmp_ne_u32_e32 vcc, 0, v154
	s_nop 1
	v_mov_b32_e32 v10, vcc_lo
	v_mov_b32_e32 v11, vcc_hi
	v_cmp_ne_u32_e32 vcc, 0, v155
	v_cndmask_b32_e64 v2, v2, v10, s[16:17]
	v_cndmask_b32_e64 v8, v9, v11, s[16:17]
	v_mov_b32_e32 v9, vcc_hi
	v_mov_b32_e32 v10, vcc_lo
	v_cndmask_b32_e64 v9, v8, v9, s[18:19]
	v_cndmask_b32_e64 v8, v2, v10, s[18:19]
	s_and_saveexec_b64 s[2:3], s[0:1]
	s_cbranch_execz .Lmk35_6
	global_store_dwordx2 v[4:5], v[8:9], off

.Lmk37_6:
	s_or_b64 exec, exec, s[2:3]
	s_waitcnt lgkmcnt(0)
	s_barrier
	s_and_saveexec_b64 s[2:3], s[4:5]
	s_cbranch_execz .Lmk32_6
	ds_read_b128 v[8:11], v3 offset:32
	ds_read_b128 v[12:15], v3
	ds_read_b128 v[16:19], v3 offset:16
	ds_read_b128 v[20:23], v3 offset:48
	s_waitcnt lgkmcnt(3)
	v_or_b32_e32 v2, v9, v8
	s_waitcnt lgkmcnt(2)
	v_or_b32_e32 v8, v13, v12
	v_or_b32_e32 v8, v8, v14
	v_or_b32_e32 v2, v2, v10
	v_or_b32_e32 v8, v8, v15
	v_or_b32_e32 v2, v2, v11
	s_waitcnt lgkmcnt(1)
	v_or_b32_e32 v8, v8, v16
	s_waitcnt lgkmcnt(0)
	v_or_b32_e32 v2, v2, v20
	v_or_b32_e32 v8, v8, v17
	v_or_b32_e32 v2, v2, v21
	v_or_b32_e32 v8, v8, v18
	v_or_b32_e32 v2, v2, v22
	v_or_b32_e32 v8, v8, v19
	v_or_b32_e32 v2, v2, v23
	v_cmp_ne_u32_e32 vcc, 0, v8
	s_nop 1
	v_cndmask_b32_e64 v8, 0, 1, vcc
	v_cmp_eq_u32_e32 vcc, 0, v2
	s_nop 1
	v_cndmask_b32_e64 v2, 2, 0, vcc
	v_or_b32_e32 v2, v2, v8
	global_store_dword v3, v2, s[26:27] offset:24
.Lmk32_6:
	s_or_b64 exec, exec, s[2:3]
	v_lshl_add_u64 v[4:5], v[4:5], 0, 8
	s_barrier
	global_load_dword v204, v96, s[60:61] offset:3328 nt
	global_load_dword v205, v96, s[62:63] offset:3328 nt
	global_load_dword v206, v96, s[64:65] offset:3328 nt
	global_load_dword v207, v96, s[66:67] offset:3328 nt
	global_load_dword v208, v96, s[68:69] offset:3328 nt
	global_load_dword v209, v96, s[70:71] offset:3328 nt
	global_load_dword v210, v96, s[72:73] offset:3328 nt
	global_load_dword v211, v96, s[74:75] offset:3328 nt
	s_waitcnt vmcnt(54)
	v_cmp_ne_u32_e32 vcc, 0, v156
	s_nop 1
	v_mov_b32_e32 v2, vcc_lo
	v_mov_b32_e32 v9, vcc_hi
	v_cmp_ne_u32_e32 vcc, 0, v157
	v_cndmask_b32_e64 v2, 0, v2, s[22:23]
	v_cndmask_b32_e64 v9, 0, v9, s[22:23]
	v_mov_b32_e32 v11, vcc_hi
	v_mov_b32_e32 v14, vcc_lo
	v_cndmask_b32_e64 v9, v9, v11, s[6:7]
	v_cndmask_b32_e64 v2, v2, v14, s[6:7]
	v_cmp_ne_u32_e32 vcc, 0, v158
	s_nop 1
	v_mov_b32_e32 v11, vcc_lo
	v_mov_b32_e32 v14, vcc_hi
	v_cmp_ne_u32_e32 vcc, 0, v159
	v_cndmask_b32_e64 v2, v2, v11, s[8:9]
	v_cndmask_b32_e64 v9, v9, v14, s[8:9]
	v_mov_b32_e32 v11, vcc_hi
	v_mov_b32_e32 v14, vcc_lo
	v_cmp_ne_u32_e32 vcc, 0, v160
	v_cndmask_b32_e64 v9, v9, v11, s[10:11]
	v_cndmask_b32_e64 v2, v2, v14, s[10:11]
	v_mov_b32_e32 v11, vcc_lo
	v_mov_b32_e32 v12, vcc_hi
	v_cmp_ne_u32_e32 vcc, 0, v161
	v_cndmask_b32_e64 v2, v2, v11, s[12:13]
	v_cndmask_b32_e64 v9, v9, v12, s[12:13]
	v_mov_b32_e32 v11, vcc_hi
	v_mov_b32_e32 v12, vcc_lo
	v_cndmask_b32_e64 v9, v9, v11, s[14:15]
	v_cndmask_b32_e64 v2, v2, v12, s[14:15]
	v_cmp_ne_u32_e32 vcc, 0, v162
	s_nop 1
	v_mov_b32_e32 v10, vcc_lo
	v_mov_b32_e32 v11, vcc_hi
	v_cmp_ne_u32_e32 vcc, 0, v163
	v_cndmask_b32_e64 v2, v2, v10, s[16:17]
	v_cndmask_b32_e64 v8, v9, v11, s[16:17]
	v_mov_b32_e32 v9, vcc_hi
	v_mov_b32_e32 v10, vcc_lo
	v_cndmask_b32_e64 v9, v8, v9, s[18:19]
	v_cndmask_b32_e64 v8, v2, v10, s[18:19]
	s_and_saveexec_b64 s[2:3], s[0:1]
	s_cbranch_execz .Lmk35_7
	global_store_dwordx2 v[4:5], v[8:9], off

.Lmk37_7:
	s_or_b64 exec, exec, s[2:3]
	s_waitcnt lgkmcnt(0)
	s_barrier
	s_and_saveexec_b64 s[2:3], s[4:5]
	s_cbranch_execz .Lmk32_7
	ds_read_b128 v[8:11], v3 offset:32
	ds_read_b128 v[12:15], v3
	ds_read_b128 v[16:19], v3 offset:16
	ds_read_b128 v[20:23], v3 offset:48
	s_waitcnt lgkmcnt(3)
	v_or_b32_e32 v2, v9, v8
	s_waitcnt lgkmcnt(2)
	v_or_b32_e32 v8, v13, v12
	v_or_b32_e32 v8, v8, v14
	v_or_b32_e32 v2, v2, v10
	v_or_b32_e32 v8, v8, v15
	v_or_b32_e32 v2, v2, v11
	s_waitcnt lgkmcnt(1)
	v_or_b32_e32 v8, v8, v16
	s_waitcnt lgkmcnt(0)
	v_or_b32_e32 v2, v2, v20
	v_or_b32_e32 v8, v8, v17
	v_or_b32_e32 v2, v2, v21
	v_or_b32_e32 v8, v8, v18
	v_or_b32_e32 v2, v2, v22
	v_or_b32_e32 v8, v8, v19
	v_or_b32_e32 v2, v2, v23
	v_cmp_ne_u32_e32 vcc, 0, v8
	s_nop 1
	v_cndmask_b32_e64 v8, 0, 1, vcc
	v_cmp_eq_u32_e32 vcc, 0, v2
	s_nop 1
	v_cndmask_b32_e64 v2, 2, 0, vcc
	v_or_b32_e32 v2, v2, v8
	global_store_dword v3, v2, s[26:27] offset:28
.Lmk32_7:
	s_or_b64 exec, exec, s[2:3]
	v_lshl_add_u64 v[4:5], v[4:5], 0, 8
	s_barrier
	global_load_dword v212, v96, s[60:61] offset:3584 nt
	global_load_dword v213, v96, s[62:63] offset:3584 nt
	global_load_dword v214, v96, s[64:65] offset:3584 nt
	global_load_dword v215, v96, s[66:67] offset:3584 nt
	global_load_dword v216, v96, s[68:69] offset:3584 nt
	global_load_dword v217, v96, s[70:71] offset:3584 nt
	global_load_dword v218, v96, s[72:73] offset:3584 nt
	global_load_dword v219, v96, s[74:75] offset:3584 nt
	s_waitcnt vmcnt(54)
	v_cmp_ne_u32_e32 vcc, 0, v164
	s_nop 1
	v_mov_b32_e32 v2, vcc_lo
	v_mov_b32_e32 v9, vcc_hi
	v_cmp_ne_u32_e32 vcc, 0, v165
	v_cndmask_b32_e64 v2, 0, v2, s[22:23]
	v_cndmask_b32_e64 v9, 0, v9, s[22:23]
	v_mov_b32_e32 v11, vcc_hi
	v_mov_b32_e32 v14, vcc_lo
	v_cndmask_b32_e64 v9, v9, v11, s[6:7]
	v_cndmask_b32_e64 v2, v2, v14, s[6:7]
	v_cmp_ne_u32_e32 vcc, 0, v166
	s_nop 1
	v_mov_b32_e32 v11, vcc_lo
	v_mov_b32_e32 v14, vcc_hi
	v_cmp_ne_u32_e32 vcc, 0, v167
	v_cndmask_b32_e64 v2, v2, v11, s[8:9]
	v_cndmask_b32_e64 v9, v9, v14, s[8:9]
	v_mov_b32_e32 v11, vcc_hi
	v_mov_b32_e32 v14, vcc_lo
	v_cmp_ne_u32_e32 vcc, 0, v168
	v_cndmask_b32_e64 v9, v9, v11, s[10:11]
	v_cndmask_b32_e64 v2, v2, v14, s[10:11]
	v_mov_b32_e32 v11, vcc_lo
	v_mov_b32_e32 v12, vcc_hi
	v_cmp_ne_u32_e32 vcc, 0, v169
	v_cndmask_b32_e64 v2, v2, v11, s[12:13]
	v_cndmask_b32_e64 v9, v9, v12, s[12:13]
	v_mov_b32_e32 v11, vcc_hi
	v_mov_b32_e32 v12, vcc_lo
	v_cndmask_b32_e64 v9, v9, v11, s[14:15]
	v_cndmask_b32_e64 v2, v2, v12, s[14:15]
	v_cmp_ne_u32_e32 vcc, 0, v170
	s_nop 1
	v_mov_b32_e32 v10, vcc_lo
	v_mov_b32_e32 v11, vcc_hi
	v_cmp_ne_u32_e32 vcc, 0, v171
	v_cndmask_b32_e64 v2, v2, v10, s[16:17]
	v_cndmask_b32_e64 v8, v9, v11, s[16:17]
	v_mov_b32_e32 v9, vcc_hi
	v_mov_b32_e32 v10, vcc_lo
	v_cndmask_b32_e64 v9, v8, v9, s[18:19]
	v_cndmask_b32_e64 v8, v2, v10, s[18:19]
	s_and_saveexec_b64 s[2:3], s[0:1]
	s_cbranch_execz .Lmk35_8
	global_store_dwordx2 v[4:5], v[8:9], off

.Lmk37_8:
	s_or_b64 exec, exec, s[2:3]
	s_waitcnt lgkmcnt(0)
	s_barrier
	s_and_saveexec_b64 s[2:3], s[4:5]
	s_cbranch_execz .Lmk32_8
	ds_read_b128 v[8:11], v3 offset:32
	ds_read_b128 v[12:15], v3
	ds_read_b128 v[16:19], v3 offset:16
	ds_read_b128 v[20:23], v3 offset:48
	s_waitcnt lgkmcnt(3)
	v_or_b32_e32 v2, v9, v8
	s_waitcnt lgkmcnt(2)
	v_or_b32_e32 v8, v13, v12
	v_or_b32_e32 v8, v8, v14
	v_or_b32_e32 v2, v2, v10
	v_or_b32_e32 v8, v8, v15
	v_or_b32_e32 v2, v2, v11
	s_waitcnt lgkmcnt(1)
	v_or_b32_e32 v8, v8, v16
	s_waitcnt lgkmcnt(0)
	v_or_b32_e32 v2, v2, v20
	v_or_b32_e32 v8, v8, v17
	v_or_b32_e32 v2, v2, v21
	v_or_b32_e32 v8, v8, v18
	v_or_b32_e32 v2, v2, v22
	v_or_b32_e32 v8, v8, v19
	v_or_b32_e32 v2, v2, v23
	v_cmp_ne_u32_e32 vcc, 0, v8
	s_nop 1
	v_cndmask_b32_e64 v8, 0, 1, vcc
	v_cmp_eq_u32_e32 vcc, 0, v2
	s_nop 1
	v_cndmask_b32_e64 v2, 2, 0, vcc
	v_or_b32_e32 v2, v2, v8
	global_store_dword v3, v2, s[26:27] offset:32
.Lmk32_8:
	s_or_b64 exec, exec, s[2:3]
	v_lshl_add_u64 v[4:5], v[4:5], 0, 8
	s_barrier
	global_load_dword v220, v96, s[60:61] offset:3840 nt
	global_load_dword v221, v96, s[62:63] offset:3840 nt
	global_load_dword v222, v96, s[64:65] offset:3840 nt
	global_load_dword v223, v96, s[66:67] offset:3840 nt
	global_load_dword v224, v96, s[68:69] offset:3840 nt
	global_load_dword v225, v96, s[70:71] offset:3840 nt
	global_load_dword v226, v96, s[72:73] offset:3840 nt
	global_load_dword v227, v96, s[74:75] offset:3840 nt
	s_waitcnt vmcnt(54)
	v_cmp_ne_u32_e32 vcc, 0, v172
	s_nop 1
	v_mov_b32_e32 v2, vcc_lo
	v_mov_b32_e32 v9, vcc_hi
	v_cmp_ne_u32_e32 vcc, 0, v173
	v_cndmask_b32_e64 v2, 0, v2, s[22:23]
	v_cndmask_b32_e64 v9, 0, v9, s[22:23]
	v_mov_b32_e32 v11, vcc_hi
	v_mov_b32_e32 v14, vcc_lo
	v_cndmask_b32_e64 v9, v9, v11, s[6:7]
	v_cndmask_b32_e64 v2, v2, v14, s[6:7]
	v_cmp_ne_u32_e32 vcc, 0, v174
	s_nop 1
	v_mov_b32_e32 v11, vcc_lo
	v_mov_b32_e32 v14, vcc_hi
	v_cmp_ne_u32_e32 vcc, 0, v175
	v_cndmask_b32_e64 v2, v2, v11, s[8:9]
	v_cndmask_b32_e64 v9, v9, v14, s[8:9]
	v_mov_b32_e32 v11, vcc_hi
	v_mov_b32_e32 v14, vcc_lo
	v_cmp_ne_u32_e32 vcc, 0, v176
	v_cndmask_b32_e64 v9, v9, v11, s[10:11]
	v_cndmask_b32_e64 v2, v2, v14, s[10:11]
	v_mov_b32_e32 v11, vcc_lo
	v_mov_b32_e32 v12, vcc_hi
	v_cmp_ne_u32_e32 vcc, 0, v177
	v_cndmask_b32_e64 v2, v2, v11, s[12:13]
	v_cndmask_b32_e64 v9, v9, v12, s[12:13]
	v_mov_b32_e32 v11, vcc_hi
	v_mov_b32_e32 v12, vcc_lo
	v_cndmask_b32_e64 v9, v9, v11, s[14:15]
	v_cndmask_b32_e64 v2, v2, v12, s[14:15]
	v_cmp_ne_u32_e32 vcc, 0, v178
	s_nop 1
	v_mov_b32_e32 v10, vcc_lo
	v_mov_b32_e32 v11, vcc_hi
	v_cmp_ne_u32_e32 vcc, 0, v179
	v_cndmask_b32_e64 v2, v2, v10, s[16:17]
	v_cndmask_b32_e64 v8, v9, v11, s[16:17]
	v_mov_b32_e32 v9, vcc_hi
	v_mov_b32_e32 v10, vcc_lo
	v_cndmask_b32_e64 v9, v8, v9, s[18:19]
	v_cndmask_b32_e64 v8, v2, v10, s[18:19]
	s_and_saveexec_b64 s[2:3], s[0:1]
	s_cbranch_execz .Lmk35_9
	global_store_dwordx2 v[4:5], v[8:9], off

.Lmk37_9:
	s_or_b64 exec, exec, s[2:3]
	s_waitcnt lgkmcnt(0)
	s_barrier
	s_and_saveexec_b64 s[2:3], s[4:5]
	s_cbranch_execz .Lmk32_9
	ds_read_b128 v[8:11], v3 offset:32
	ds_read_b128 v[12:15], v3
	ds_read_b128 v[16:19], v3 offset:16
	ds_read_b128 v[20:23], v3 offset:48
	s_waitcnt lgkmcnt(3)
	v_or_b32_e32 v2, v9, v8
	s_waitcnt lgkmcnt(2)
	v_or_b32_e32 v8, v13, v12
	v_or_b32_e32 v8, v8, v14
	v_or_b32_e32 v2, v2, v10
	v_or_b32_e32 v8, v8, v15
	v_or_b32_e32 v2, v2, v11
	s_waitcnt lgkmcnt(1)
	v_or_b32_e32 v8, v8, v16
	s_waitcnt lgkmcnt(0)
	v_or_b32_e32 v2, v2, v20
	v_or_b32_e32 v8, v8, v17
	v_or_b32_e32 v2, v2, v21
	v_or_b32_e32 v8, v8, v18
	v_or_b32_e32 v2, v2, v22
	v_or_b32_e32 v8, v8, v19
	v_or_b32_e32 v2, v2, v23
	v_cmp_ne_u32_e32 vcc, 0, v8
	s_nop 1
	v_cndmask_b32_e64 v8, 0, 1, vcc
	v_cmp_eq_u32_e32 vcc, 0, v2
	s_nop 1
	v_cndmask_b32_e64 v2, 2, 0, vcc
	v_or_b32_e32 v2, v2, v8
	global_store_dword v3, v2, s[26:27] offset:36
.Lmk32_9:
	s_or_b64 exec, exec, s[2:3]
	v_lshl_add_u64 v[4:5], v[4:5], 0, 8
	s_barrier
	s_waitcnt vmcnt(46)
	v_cmp_ne_u32_e32 vcc, 0, v180
	s_nop 1
	v_mov_b32_e32 v2, vcc_lo
	v_mov_b32_e32 v9, vcc_hi
	v_cmp_ne_u32_e32 vcc, 0, v181
	v_cndmask_b32_e64 v2, 0, v2, s[22:23]
	v_cndmask_b32_e64 v9, 0, v9, s[22:23]
	v_mov_b32_e32 v11, vcc_hi
	v_mov_b32_e32 v14, vcc_lo
	v_cndmask_b32_e64 v9, v9, v11, s[6:7]
	v_cndmask_b32_e64 v2, v2, v14, s[6:7]
	v_cmp_ne_u32_e32 vcc, 0, v182
	s_nop 1
	v_mov_b32_e32 v11, vcc_lo
	v_mov_b32_e32 v14, vcc_hi
	v_cmp_ne_u32_e32 vcc, 0, v183
	v_cndmask_b32_e64 v2, v2, v11, s[8:9]
	v_cndmask_b32_e64 v9, v9, v14, s[8:9]
	v_mov_b32_e32 v11, vcc_hi
	v_mov_b32_e32 v14, vcc_lo
	v_cmp_ne_u32_e32 vcc, 0, v184
	v_cndmask_b32_e64 v9, v9, v11, s[10:11]
	v_cndmask_b32_e64 v2, v2, v14, s[10:11]
	v_mov_b32_e32 v11, vcc_lo
	v_mov_b32_e32 v12, vcc_hi
	v_cmp_ne_u32_e32 vcc, 0, v185
	v_cndmask_b32_e64 v2, v2, v11, s[12:13]
	v_cndmask_b32_e64 v9, v9, v12, s[12:13]
	v_mov_b32_e32 v11, vcc_hi
	v_mov_b32_e32 v12, vcc_lo
	v_cndmask_b32_e64 v9, v9, v11, s[14:15]
	v_cndmask_b32_e64 v2, v2, v12, s[14:15]
	v_cmp_ne_u32_e32 vcc, 0, v186
	s_nop 1
	v_mov_b32_e32 v10, vcc_lo
	v_mov_b32_e32 v11, vcc_hi
	v_cmp_ne_u32_e32 vcc, 0, v187
	v_cndmask_b32_e64 v2, v2, v10, s[16:17]
	v_cndmask_b32_e64 v8, v9, v11, s[16:17]
	v_mov_b32_e32 v9, vcc_hi
	v_mov_b32_e32 v10, vcc_lo
	v_cndmask_b32_e64 v9, v8, v9, s[18:19]
	v_cndmask_b32_e64 v8, v2, v10, s[18:19]
	s_and_saveexec_b64 s[2:3], s[0:1]
	s_cbranch_execz .Lmk35_10
	global_store_dwordx2 v[4:5], v[8:9], off

.Lmk37_10:
	s_or_b64 exec, exec, s[2:3]
	s_waitcnt lgkmcnt(0)
	s_barrier
	s_and_saveexec_b64 s[2:3], s[4:5]
	s_cbranch_execz .Lmk32_10
	ds_read_b128 v[8:11], v3 offset:32
	ds_read_b128 v[12:15], v3
	ds_read_b128 v[16:19], v3 offset:16
	ds_read_b128 v[20:23], v3 offset:48
	s_waitcnt lgkmcnt(3)
	v_or_b32_e32 v2, v9, v8
	s_waitcnt lgkmcnt(2)
	v_or_b32_e32 v8, v13, v12
	v_or_b32_e32 v8, v8, v14
	v_or_b32_e32 v2, v2, v10
	v_or_b32_e32 v8, v8, v15
	v_or_b32_e32 v2, v2, v11
	s_waitcnt lgkmcnt(1)
	v_or_b32_e32 v8, v8, v16
	s_waitcnt lgkmcnt(0)
	v_or_b32_e32 v2, v2, v20
	v_or_b32_e32 v8, v8, v17
	v_or_b32_e32 v2, v2, v21
	v_or_b32_e32 v8, v8, v18
	v_or_b32_e32 v2, v2, v22
	v_or_b32_e32 v8, v8, v19
	v_or_b32_e32 v2, v2, v23
	v_cmp_ne_u32_e32 vcc, 0, v8
	s_nop 1
	v_cndmask_b32_e64 v8, 0, 1, vcc
	v_cmp_eq_u32_e32 vcc, 0, v2
	s_nop 1
	v_cndmask_b32_e64 v2, 2, 0, vcc
	v_or_b32_e32 v2, v2, v8
	global_store_dword v3, v2, s[26:27] offset:40
.Lmk32_10:
	s_or_b64 exec, exec, s[2:3]
	v_lshl_add_u64 v[4:5], v[4:5], 0, 8
	s_barrier
	s_waitcnt vmcnt(38)
	v_cmp_ne_u32_e32 vcc, 0, v188
	s_nop 1
	v_mov_b32_e32 v2, vcc_lo
	v_mov_b32_e32 v9, vcc_hi
	v_cmp_ne_u32_e32 vcc, 0, v189
	v_cndmask_b32_e64 v2, 0, v2, s[22:23]
	v_cndmask_b32_e64 v9, 0, v9, s[22:23]
	v_mov_b32_e32 v11, vcc_hi
	v_mov_b32_e32 v14, vcc_lo
	v_cndmask_b32_e64 v9, v9, v11, s[6:7]
	v_cndmask_b32_e64 v2, v2, v14, s[6:7]
	v_cmp_ne_u32_e32 vcc, 0, v190
	s_nop 1
	v_mov_b32_e32 v11, vcc_lo
	v_mov_b32_e32 v14, vcc_hi
	v_cmp_ne_u32_e32 vcc, 0, v191
	v_cndmask_b32_e64 v2, v2, v11, s[8:9]
	v_cndmask_b32_e64 v9, v9, v14, s[8:9]
	v_mov_b32_e32 v11, vcc_hi
	v_mov_b32_e32 v14, vcc_lo
	v_cmp_ne_u32_e32 vcc, 0, v192
	v_cndmask_b32_e64 v9, v9, v11, s[10:11]
	v_cndmask_b32_e64 v2, v2, v14, s[10:11]
	v_mov_b32_e32 v11, vcc_lo
	v_mov_b32_e32 v12, vcc_hi
	v_cmp_ne_u32_e32 vcc, 0, v193
	v_cndmask_b32_e64 v2, v2, v11, s[12:13]
	v_cndmask_b32_e64 v9, v9, v12, s[12:13]
	v_mov_b32_e32 v11, vcc_hi
	v_mov_b32_e32 v12, vcc_lo
	v_cndmask_b32_e64 v9, v9, v11, s[14:15]
	v_cndmask_b32_e64 v2, v2, v12, s[14:15]
	v_cmp_ne_u32_e32 vcc, 0, v194
	s_nop 1
	v_mov_b32_e32 v10, vcc_lo
	v_mov_b32_e32 v11, vcc_hi
	v_cmp_ne_u32_e32 vcc, 0, v195
	v_cndmask_b32_e64 v2, v2, v10, s[16:17]
	v_cndmask_b32_e64 v8, v9, v11, s[16:17]
	v_mov_b32_e32 v9, vcc_hi
	v_mov_b32_e32 v10, vcc_lo
	v_cndmask_b32_e64 v9, v8, v9, s[18:19]
	v_cndmask_b32_e64 v8, v2, v10, s[18:19]
	s_and_saveexec_b64 s[2:3], s[0:1]
	s_cbranch_execz .Lmk35_11
	global_store_dwordx2 v[4:5], v[8:9], off

.Lmk37_11:
	s_or_b64 exec, exec, s[2:3]
	s_waitcnt lgkmcnt(0)
	s_barrier
	s_and_saveexec_b64 s[2:3], s[4:5]
	s_cbranch_execz .Lmk32_11
	ds_read_b128 v[8:11], v3 offset:32
	ds_read_b128 v[12:15], v3
	ds_read_b128 v[16:19], v3 offset:16
	ds_read_b128 v[20:23], v3 offset:48
	s_waitcnt lgkmcnt(3)
	v_or_b32_e32 v2, v9, v8
	s_waitcnt lgkmcnt(2)
	v_or_b32_e32 v8, v13, v12
	v_or_b32_e32 v8, v8, v14
	v_or_b32_e32 v2, v2, v10
	v_or_b32_e32 v8, v8, v15
	v_or_b32_e32 v2, v2, v11
	s_waitcnt lgkmcnt(1)
	v_or_b32_e32 v8, v8, v16
	s_waitcnt lgkmcnt(0)
	v_or_b32_e32 v2, v2, v20
	v_or_b32_e32 v8, v8, v17
	v_or_b32_e32 v2, v2, v21
	v_or_b32_e32 v8, v8, v18
	v_or_b32_e32 v2, v2, v22
	v_or_b32_e32 v8, v8, v19
	v_or_b32_e32 v2, v2, v23
	v_cmp_ne_u32_e32 vcc, 0, v8
	s_nop 1
	v_cndmask_b32_e64 v8, 0, 1, vcc
	v_cmp_eq_u32_e32 vcc, 0, v2
	s_nop 1
	v_cndmask_b32_e64 v2, 2, 0, vcc
	v_or_b32_e32 v2, v2, v8
	global_store_dword v3, v2, s[26:27] offset:44
.Lmk32_11:
	s_or_b64 exec, exec, s[2:3]
	v_lshl_add_u64 v[4:5], v[4:5], 0, 8
	s_barrier
	s_waitcnt vmcnt(30)
	v_cmp_ne_u32_e32 vcc, 0, v196
	s_nop 1
	v_mov_b32_e32 v2, vcc_lo
	v_mov_b32_e32 v9, vcc_hi
	v_cmp_ne_u32_e32 vcc, 0, v197
	v_cndmask_b32_e64 v2, 0, v2, s[22:23]
	v_cndmask_b32_e64 v9, 0, v9, s[22:23]
	v_mov_b32_e32 v11, vcc_hi
	v_mov_b32_e32 v14, vcc_lo
	v_cndmask_b32_e64 v9, v9, v11, s[6:7]
	v_cndmask_b32_e64 v2, v2, v14, s[6:7]
	v_cmp_ne_u32_e32 vcc, 0, v198
	s_nop 1
	v_mov_b32_e32 v11, vcc_lo
	v_mov_b32_e32 v14, vcc_hi
	v_cmp_ne_u32_e32 vcc, 0, v199
	v_cndmask_b32_e64 v2, v2, v11, s[8:9]
	v_cndmask_b32_e64 v9, v9, v14, s[8:9]
	v_mov_b32_e32 v11, vcc_hi
	v_mov_b32_e32 v14, vcc_lo
	v_cmp_ne_u32_e32 vcc, 0, v200
	v_cndmask_b32_e64 v9, v9, v11, s[10:11]
	v_cndmask_b32_e64 v2, v2, v14, s[10:11]
	v_mov_b32_e32 v11, vcc_lo
	v_mov_b32_e32 v12, vcc_hi
	v_cmp_ne_u32_e32 vcc, 0, v201
	v_cndmask_b32_e64 v2, v2, v11, s[12:13]
	v_cndmask_b32_e64 v9, v9, v12, s[12:13]
	v_mov_b32_e32 v11, vcc_hi
	v_mov_b32_e32 v12, vcc_lo
	v_cndmask_b32_e64 v9, v9, v11, s[14:15]
	v_cndmask_b32_e64 v2, v2, v12, s[14:15]
	v_cmp_ne_u32_e32 vcc, 0, v202
	s_nop 1
	v_mov_b32_e32 v10, vcc_lo
	v_mov_b32_e32 v11, vcc_hi
	v_cmp_ne_u32_e32 vcc, 0, v203
	v_cndmask_b32_e64 v2, v2, v10, s[16:17]
	v_cndmask_b32_e64 v8, v9, v11, s[16:17]
	v_mov_b32_e32 v9, vcc_hi
	v_mov_b32_e32 v10, vcc_lo
	v_cndmask_b32_e64 v9, v8, v9, s[18:19]
	v_cndmask_b32_e64 v8, v2, v10, s[18:19]
	s_and_saveexec_b64 s[2:3], s[0:1]
	s_cbranch_execz .Lmk35_12
	global_store_dwordx2 v[4:5], v[8:9], off

.Lmk37_12:
	s_or_b64 exec, exec, s[2:3]
	s_waitcnt lgkmcnt(0)
	s_barrier
	s_and_saveexec_b64 s[2:3], s[4:5]
	s_cbranch_execz .Lmk32_12
	ds_read_b128 v[8:11], v3 offset:32
	ds_read_b128 v[12:15], v3
	ds_read_b128 v[16:19], v3 offset:16
	ds_read_b128 v[20:23], v3 offset:48
	s_waitcnt lgkmcnt(3)
	v_or_b32_e32 v2, v9, v8
	s_waitcnt lgkmcnt(2)
	v_or_b32_e32 v8, v13, v12
	v_or_b32_e32 v8, v8, v14
	v_or_b32_e32 v2, v2, v10
	v_or_b32_e32 v8, v8, v15
	v_or_b32_e32 v2, v2, v11
	s_waitcnt lgkmcnt(1)
	v_or_b32_e32 v8, v8, v16
	s_waitcnt lgkmcnt(0)
	v_or_b32_e32 v2, v2, v20
	v_or_b32_e32 v8, v8, v17
	v_or_b32_e32 v2, v2, v21
	v_or_b32_e32 v8, v8, v18
	v_or_b32_e32 v2, v2, v22
	v_or_b32_e32 v8, v8, v19
	v_or_b32_e32 v2, v2, v23
	v_cmp_ne_u32_e32 vcc, 0, v8
	s_nop 1
	v_cndmask_b32_e64 v8, 0, 1, vcc
	v_cmp_eq_u32_e32 vcc, 0, v2
	s_nop 1
	v_cndmask_b32_e64 v2, 2, 0, vcc
	v_or_b32_e32 v2, v2, v8
	global_store_dword v3, v2, s[26:27] offset:48
.Lmk32_12:
	s_or_b64 exec, exec, s[2:3]
	v_lshl_add_u64 v[4:5], v[4:5], 0, 8
	s_barrier
	s_waitcnt vmcnt(22)
	v_cmp_ne_u32_e32 vcc, 0, v204
	s_nop 1
	v_mov_b32_e32 v2, vcc_lo
	v_mov_b32_e32 v9, vcc_hi
	v_cmp_ne_u32_e32 vcc, 0, v205
	v_cndmask_b32_e64 v2, 0, v2, s[22:23]
	v_cndmask_b32_e64 v9, 0, v9, s[22:23]
	v_mov_b32_e32 v11, vcc_hi
	v_mov_b32_e32 v14, vcc_lo
	v_cndmask_b32_e64 v9, v9, v11, s[6:7]
	v_cndmask_b32_e64 v2, v2, v14, s[6:7]
	v_cmp_ne_u32_e32 vcc, 0, v206
	s_nop 1
	v_mov_b32_e32 v11, vcc_lo
	v_mov_b32_e32 v14, vcc_hi
	v_cmp_ne_u32_e32 vcc, 0, v207
	v_cndmask_b32_e64 v2, v2, v11, s[8:9]
	v_cndmask_b32_e64 v9, v9, v14, s[8:9]
	v_mov_b32_e32 v11, vcc_hi
	v_mov_b32_e32 v14, vcc_lo
	v_cmp_ne_u32_e32 vcc, 0, v208
	v_cndmask_b32_e64 v9, v9, v11, s[10:11]
	v_cndmask_b32_e64 v2, v2, v14, s[10:11]
	v_mov_b32_e32 v11, vcc_lo
	v_mov_b32_e32 v12, vcc_hi
	v_cmp_ne_u32_e32 vcc, 0, v209
	v_cndmask_b32_e64 v2, v2, v11, s[12:13]
	v_cndmask_b32_e64 v9, v9, v12, s[12:13]
	v_mov_b32_e32 v11, vcc_hi
	v_mov_b32_e32 v12, vcc_lo
	v_cndmask_b32_e64 v9, v9, v11, s[14:15]
	v_cndmask_b32_e64 v2, v2, v12, s[14:15]
	v_cmp_ne_u32_e32 vcc, 0, v210
	s_nop 1
	v_mov_b32_e32 v10, vcc_lo
	v_mov_b32_e32 v11, vcc_hi
	v_cmp_ne_u32_e32 vcc, 0, v211
	v_cndmask_b32_e64 v2, v2, v10, s[16:17]
	v_cndmask_b32_e64 v8, v9, v11, s[16:17]
	v_mov_b32_e32 v9, vcc_hi
	v_mov_b32_e32 v10, vcc_lo
	v_cndmask_b32_e64 v9, v8, v9, s[18:19]
	v_cndmask_b32_e64 v8, v2, v10, s[18:19]
	s_and_saveexec_b64 s[2:3], s[0:1]
	s_cbranch_execz .Lmk35_13
	global_store_dwordx2 v[4:5], v[8:9], off

.Lmk37_13:
	s_or_b64 exec, exec, s[2:3]
	s_waitcnt lgkmcnt(0)
	s_barrier
	s_and_saveexec_b64 s[2:3], s[4:5]
	s_cbranch_execz .Lmk32_13
	ds_read_b128 v[8:11], v3 offset:32
	ds_read_b128 v[12:15], v3
	ds_read_b128 v[16:19], v3 offset:16
	ds_read_b128 v[20:23], v3 offset:48
	s_waitcnt lgkmcnt(3)
	v_or_b32_e32 v2, v9, v8
	s_waitcnt lgkmcnt(2)
	v_or_b32_e32 v8, v13, v12
	v_or_b32_e32 v8, v8, v14
	v_or_b32_e32 v2, v2, v10
	v_or_b32_e32 v8, v8, v15
	v_or_b32_e32 v2, v2, v11
	s_waitcnt lgkmcnt(1)
	v_or_b32_e32 v8, v8, v16
	s_waitcnt lgkmcnt(0)
	v_or_b32_e32 v2, v2, v20
	v_or_b32_e32 v8, v8, v17
	v_or_b32_e32 v2, v2, v21
	v_or_b32_e32 v8, v8, v18
	v_or_b32_e32 v2, v2, v22
	v_or_b32_e32 v8, v8, v19
	v_or_b32_e32 v2, v2, v23
	v_cmp_ne_u32_e32 vcc, 0, v8
	s_nop 1
	v_cndmask_b32_e64 v8, 0, 1, vcc
	v_cmp_eq_u32_e32 vcc, 0, v2
	s_nop 1
	v_cndmask_b32_e64 v2, 2, 0, vcc
	v_or_b32_e32 v2, v2, v8
	global_store_dword v3, v2, s[26:27] offset:52
.Lmk32_13:
	s_or_b64 exec, exec, s[2:3]
	v_lshl_add_u64 v[4:5], v[4:5], 0, 8
	s_barrier
	s_waitcnt vmcnt(14)
	v_cmp_ne_u32_e32 vcc, 0, v212
	s_nop 1
	v_mov_b32_e32 v2, vcc_lo
	v_mov_b32_e32 v9, vcc_hi
	v_cmp_ne_u32_e32 vcc, 0, v213
	v_cndmask_b32_e64 v2, 0, v2, s[22:23]
	v_cndmask_b32_e64 v9, 0, v9, s[22:23]
	v_mov_b32_e32 v11, vcc_hi
	v_mov_b32_e32 v14, vcc_lo
	v_cndmask_b32_e64 v9, v9, v11, s[6:7]
	v_cndmask_b32_e64 v2, v2, v14, s[6:7]
	v_cmp_ne_u32_e32 vcc, 0, v214
	s_nop 1
	v_mov_b32_e32 v11, vcc_lo
	v_mov_b32_e32 v14, vcc_hi
	v_cmp_ne_u32_e32 vcc, 0, v215
	v_cndmask_b32_e64 v2, v2, v11, s[8:9]
	v_cndmask_b32_e64 v9, v9, v14, s[8:9]
	v_mov_b32_e32 v11, vcc_hi
	v_mov_b32_e32 v14, vcc_lo
	v_cmp_ne_u32_e32 vcc, 0, v216
	v_cndmask_b32_e64 v9, v9, v11, s[10:11]
	v_cndmask_b32_e64 v2, v2, v14, s[10:11]
	v_mov_b32_e32 v11, vcc_lo
	v_mov_b32_e32 v12, vcc_hi
	v_cmp_ne_u32_e32 vcc, 0, v217
	v_cndmask_b32_e64 v2, v2, v11, s[12:13]
	v_cndmask_b32_e64 v9, v9, v12, s[12:13]
	v_mov_b32_e32 v11, vcc_hi
	v_mov_b32_e32 v12, vcc_lo
	v_cndmask_b32_e64 v9, v9, v11, s[14:15]
	v_cndmask_b32_e64 v2, v2, v12, s[14:15]
	v_cmp_ne_u32_e32 vcc, 0, v218
	s_nop 1
	v_mov_b32_e32 v10, vcc_lo
	v_mov_b32_e32 v11, vcc_hi
	v_cmp_ne_u32_e32 vcc, 0, v219
	v_cndmask_b32_e64 v2, v2, v10, s[16:17]
	v_cndmask_b32_e64 v8, v9, v11, s[16:17]
	v_mov_b32_e32 v9, vcc_hi
	v_mov_b32_e32 v10, vcc_lo
	v_cndmask_b32_e64 v9, v8, v9, s[18:19]
	v_cndmask_b32_e64 v8, v2, v10, s[18:19]
	s_and_saveexec_b64 s[2:3], s[0:1]
	s_cbranch_execz .Lmk35_14
	global_store_dwordx2 v[4:5], v[8:9], off

.Lmk37_14:
	s_or_b64 exec, exec, s[2:3]
	s_waitcnt lgkmcnt(0)
	s_barrier
	s_and_saveexec_b64 s[2:3], s[4:5]
	s_cbranch_execz .Lmk32_14
	ds_read_b128 v[8:11], v3 offset:32
	ds_read_b128 v[12:15], v3
	ds_read_b128 v[16:19], v3 offset:16
	ds_read_b128 v[20:23], v3 offset:48
	s_waitcnt lgkmcnt(3)
	v_or_b32_e32 v2, v9, v8
	s_waitcnt lgkmcnt(2)
	v_or_b32_e32 v8, v13, v12
	v_or_b32_e32 v8, v8, v14
	v_or_b32_e32 v2, v2, v10
	v_or_b32_e32 v8, v8, v15
	v_or_b32_e32 v2, v2, v11
	s_waitcnt lgkmcnt(1)
	v_or_b32_e32 v8, v8, v16
	s_waitcnt lgkmcnt(0)
	v_or_b32_e32 v2, v2, v20
	v_or_b32_e32 v8, v8, v17
	v_or_b32_e32 v2, v2, v21
	v_or_b32_e32 v8, v8, v18
	v_or_b32_e32 v2, v2, v22
	v_or_b32_e32 v8, v8, v19
	v_or_b32_e32 v2, v2, v23
	v_cmp_ne_u32_e32 vcc, 0, v8
	s_nop 1
	v_cndmask_b32_e64 v8, 0, 1, vcc
	v_cmp_eq_u32_e32 vcc, 0, v2
	s_nop 1
	v_cndmask_b32_e64 v2, 2, 0, vcc
	v_or_b32_e32 v2, v2, v8
	global_store_dword v3, v2, s[26:27] offset:56
.Lmk32_14:
	s_or_b64 exec, exec, s[2:3]
	v_lshl_add_u64 v[4:5], v[4:5], 0, 8
	s_barrier
	s_waitcnt vmcnt(6)
	v_cmp_ne_u32_e32 vcc, 0, v220
	s_nop 1
	v_mov_b32_e32 v2, vcc_lo
	v_mov_b32_e32 v9, vcc_hi
	v_cmp_ne_u32_e32 vcc, 0, v221
	v_cndmask_b32_e64 v2, 0, v2, s[22:23]
	v_cndmask_b32_e64 v9, 0, v9, s[22:23]
	v_mov_b32_e32 v11, vcc_hi
	v_mov_b32_e32 v14, vcc_lo
	v_cndmask_b32_e64 v9, v9, v11, s[6:7]
	v_cndmask_b32_e64 v2, v2, v14, s[6:7]
	v_cmp_ne_u32_e32 vcc, 0, v222
	s_nop 1
	v_mov_b32_e32 v11, vcc_lo
	v_mov_b32_e32 v14, vcc_hi
	v_cmp_ne_u32_e32 vcc, 0, v223
	v_cndmask_b32_e64 v2, v2, v11, s[8:9]
	v_cndmask_b32_e64 v9, v9, v14, s[8:9]
	v_mov_b32_e32 v11, vcc_hi
	v_mov_b32_e32 v14, vcc_lo
	v_cmp_ne_u32_e32 vcc, 0, v224
	v_cndmask_b32_e64 v9, v9, v11, s[10:11]
	v_cndmask_b32_e64 v2, v2, v14, s[10:11]
	v_mov_b32_e32 v11, vcc_lo
	v_mov_b32_e32 v12, vcc_hi
	v_cmp_ne_u32_e32 vcc, 0, v225
	v_cndmask_b32_e64 v2, v2, v11, s[12:13]
	v_cndmask_b32_e64 v9, v9, v12, s[12:13]
	v_mov_b32_e32 v11, vcc_hi
	v_mov_b32_e32 v12, vcc_lo
	v_cndmask_b32_e64 v9, v9, v11, s[14:15]
	v_cndmask_b32_e64 v2, v2, v12, s[14:15]
	v_cmp_ne_u32_e32 vcc, 0, v226
	s_nop 1
	v_mov_b32_e32 v10, vcc_lo
	v_mov_b32_e32 v11, vcc_hi
	v_cmp_ne_u32_e32 vcc, 0, v227
	v_cndmask_b32_e64 v2, v2, v10, s[16:17]
	v_cndmask_b32_e64 v8, v9, v11, s[16:17]
	v_mov_b32_e32 v9, vcc_hi
	v_mov_b32_e32 v10, vcc_lo
	v_cndmask_b32_e64 v9, v8, v9, s[18:19]
	v_cndmask_b32_e64 v8, v2, v10, s[18:19]
	s_and_saveexec_b64 s[2:3], s[0:1]
	s_cbranch_execz .Lmk35_15
	global_store_dwordx2 v[4:5], v[8:9], off

.Lmk37_15:
	s_or_b64 exec, exec, s[2:3]
	s_waitcnt lgkmcnt(0)
	s_barrier
	s_and_saveexec_b64 s[2:3], s[4:5]
	s_cbranch_execz .Lmk32_15
	ds_read_b128 v[8:11], v3 offset:32
	ds_read_b128 v[12:15], v3
	ds_read_b128 v[16:19], v3 offset:16
	ds_read_b128 v[20:23], v3 offset:48
	s_waitcnt lgkmcnt(3)
	v_or_b32_e32 v2, v9, v8
	s_waitcnt lgkmcnt(2)
	v_or_b32_e32 v8, v13, v12
	v_or_b32_e32 v8, v8, v14
	v_or_b32_e32 v2, v2, v10
	v_or_b32_e32 v8, v8, v15
	v_or_b32_e32 v2, v2, v11
	s_waitcnt lgkmcnt(1)
	v_or_b32_e32 v8, v8, v16
	s_waitcnt lgkmcnt(0)
	v_or_b32_e32 v2, v2, v20
	v_or_b32_e32 v8, v8, v17
	v_or_b32_e32 v2, v2, v21
	v_or_b32_e32 v8, v8, v18
	v_or_b32_e32 v2, v2, v22
	v_or_b32_e32 v8, v8, v19
	v_or_b32_e32 v2, v2, v23
	v_cmp_ne_u32_e32 vcc, 0, v8
	s_nop 1
	v_cndmask_b32_e64 v8, 0, 1, vcc
	v_cmp_eq_u32_e32 vcc, 0, v2
	s_nop 1
	v_cndmask_b32_e64 v2, 2, 0, vcc
	v_or_b32_e32 v2, v2, v8
	global_store_dword v3, v2, s[26:27] offset:60
.Lmk32_15:
	s_or_b64 exec, exec, s[2:3]
	v_lshl_add_u64 v[4:5], v[4:5], 0, 8
	s_barrier

	.amdhsa_kernel _Z15gemm_qkv_kernelPKDF16_S0_PDF16_S1_S1_PKfS3_S3_S3_S3_S1_PKiPyPj
		.amdhsa_group_segment_fixed_size 0
		.amdhsa_private_segment_fixed_size 0
		.amdhsa_kernarg_size 112
		.amdhsa_user_sgpr_count 2
		.amdhsa_user_sgpr_dispatch_ptr 0
		.amdhsa_user_sgpr_queue_ptr 0
		.amdhsa_user_sgpr_kernarg_segment_ptr 1
		.amdhsa_user_sgpr_dispatch_id 0
		.amdhsa_user_sgpr_kernarg_preload_length 0
		.amdhsa_user_sgpr_kernarg_preload_offset 0
		.amdhsa_user_sgpr_private_segment_size 0
		.amdhsa_uses_dynamic_stack 0
		.amdhsa_enable_private_segment 0
		.amdhsa_system_sgpr_workgroup_id_x 1
		.amdhsa_system_sgpr_workgroup_id_y 0
		.amdhsa_system_sgpr_workgroup_id_z 0
		.amdhsa_system_sgpr_workgroup_info 0
		.amdhsa_system_vgpr_workitem_id 0
		.amdhsa_next_free_vgpr 244
		.amdhsa_next_free_sgpr 84
		.amdhsa_accum_offset 244
		.amdhsa_reserve_vcc 1
		.amdhsa_float_round_mode_32 0
		.amdhsa_float_round_mode_16_64 0
		.amdhsa_float_denorm_mode_32 3
		.amdhsa_float_denorm_mode_16_64 3
		.amdhsa_dx10_clamp 1
		.amdhsa_ieee_mode 1
		.amdhsa_fp16_overflow 0
		.amdhsa_tg_split 0
		.amdhsa_exception_fp_ieee_invalid_op 0
		.amdhsa_exception_fp_denorm_src 0
		.amdhsa_exception_fp_ieee_div_zero 0
		.amdhsa_exception_fp_ieee_overflow 0
		.amdhsa_exception_fp_ieee_underflow 0
		.amdhsa_exception_fp_ieee_inexact 0
		.amdhsa_exception_int_div_zero 0
	.end_amdhsa_kernel

amdhsa.kernels:
  - .agpr_count:     0
    .args:
      - .actual_access:  read_only
        .address_space:  global
        .offset:         0
        .size:           8
        .value_kind:     global_buffer
      - .actual_access:  read_only
        .address_space:  global
        .offset:         8
        .size:           8
        .value_kind:     global_buffer
      - .actual_access:  read_only
        .address_space:  global
        .offset:         16
        .size:           8
        .value_kind:     global_buffer
      - .actual_access:  write_only
        .address_space:  global
        .offset:         24
        .size:           8
        .value_kind:     global_buffer
      - .actual_access:  write_only
        .address_space:  global
        .offset:         32
        .size:           8
        .value_kind:     global_buffer
      - .actual_access:  write_only
        .address_space:  global
        .offset:         40
        .size:           8
        .value_kind:     global_buffer
      - .actual_access:  write_only
        .address_space:  global
        .offset:         48
        .size:           8
        .value_kind:     global_buffer
    .group_segment_fixed_size: 0
    .kernarg_segment_align: 8
    .kernarg_segment_size: 56
    .language:       OpenCL C
    .language_version:
      - 2
      - 0
    .max_flat_workgroup_size: 1024
    .name:           _Z11prep_kernelPKfS0_PKiPDF16_S3_PfS4_
    .private_segment_fixed_size: 0
    .sgpr_count:     24
    .sgpr_spill_count: 0
    .symbol:         _Z11prep_kernelPKfS0_PKiPDF16_S3_PfS4_.kd
    .uniform_work_group_size: 1
    .uses_dynamic_stack: false
    .vgpr_count:     40
    .vgpr_spill_count: 0
    .wavefront_size: 64
  - .agpr_count:     0
    .args:
      - .address_space:  global
        .offset:         0
        .size:           8
        .value_kind:     global_buffer
      - .address_space:  global
        .offset:         8
        .size:           8
        .value_kind:     global_buffer
      - .address_space:  global
        .offset:         16
        .size:           8
        .value_kind:     global_buffer
      - .address_space:  global
        .offset:         24
        .size:           8
        .value_kind:     global_buffer
      - .address_space:  global
        .offset:         32
        .size:           8
        .value_kind:     global_buffer
      - .address_space:  global
        .offset:         40
        .size:           8
        .value_kind:     global_buffer
      - .address_space:  global
        .offset:         48
        .size:           8
        .value_kind:     global_buffer
      - .address_space:  global
        .offset:         56
        .size:           8
        .value_kind:     global_buffer
      - .address_space:  global
        .offset:         64
        .size:           8
        .value_kind:     global_buffer
      - .address_space:  global
        .offset:         72
        .size:           8
        .value_kind:     global_buffer
      - .address_space:  global
        .offset:         80
        .size:           8
        .value_kind:     global_buffer
      - .address_space:  global
        .offset:         88
        .size:           8
        .value_kind:     global_buffer
      - .address_space:  global
        .offset:         96
        .size:           8
        .value_kind:     global_buffer
      - .address_space:  global
        .offset:         104
        .size:           8
        .value_kind:     global_buffer
    .group_segment_fixed_size: 0
    .kernarg_segment_align: 8
    .kernarg_segment_size: 112
    .language:       OpenCL C
    .language_version:
      - 2
      - 0
    .max_flat_workgroup_size: 512
    .name:           _Z15gemm_qkv_kernelPKDF16_S0_PDF16_S1_S1_PKfS3_S3_S3_S3_S1_PKiPyPj
    .private_segment_fixed_size: 0
    .sgpr_count:     90
    .sgpr_spill_count: 0
    .symbol:         _Z15gemm_qkv_kernelPKDF16_S0_PDF16_S1_S1_PKfS3_S3_S3_S3_S1_PKiPyPj.kd
    .uniform_work_group_size: 1
    .uses_dynamic_stack: false
    .vgpr_count:     244
    .vgpr_spill_count: 0
    .wavefront_size: 64
  - .agpr_count:     0
    .args:
      - .address_space:  global
        .offset:         0
        .size:           8
        .value_kind:     global_buffer
      - .address_space:  global
        .offset:         8
        .size:           8
        .value_kind:     global_buffer
      - .address_space:  global
        .offset:         16
        .size:           8
        .value_kind:     global_buffer
    .group_segment_fixed_size: 0
    .kernarg_segment_align: 8
    .kernarg_segment_size: 24
    .language:       OpenCL C
    .language_version:
      - 2
      - 0
    .max_flat_workgroup_size: 512
    .name:           _Z15gemm_out_kernelPKDF16_S0_Pf
    .private_segment_fixed_size: 0
    .sgpr_count:     26
    .sgpr_spill_count: 0
    .symbol:         _Z15gemm_out_kernelPKDF16_S0_Pf.kd
    .uniform_work_group_size: 1
    .uses_dynamic_stack: false
    .vgpr_count:     148
    .vgpr_spill_count: 0
    .wavefront_size: 64
  - .agpr_count:     0
    .args:
      - .address_space:  global
        .offset:         0
        .size:           8
        .value_kind:     global_buffer
      - .address_space:  global
        .offset:         8
        .size:           8
        .value_kind:     global_buffer
      - .address_space:  global
        .offset:         16
        .size:           8
        .value_kind:     global_buffer
      - .address_space:  global
        .offset:         24
        .size:           8
        .value_kind:     global_buffer
      - .address_space:  global
        .offset:         32
        .size:           8
        .value_kind:     global_buffer
      - .address_space:  global
        .offset:         40
        .size:           8
        .value_kind:     global_buffer
    .group_segment_fixed_size: 0
    .kernarg_segment_align: 8
    .kernarg_segment_size: 48
    .language:       OpenCL C
    .language_version:
      - 2
      - 0
    .max_flat_workgroup_size: 512
    .name:           _Z11attn_kernelPKDF16_S0_S0_PDF16_PKjS3_
    .private_segment_fixed_size: 0
    .sgpr_count:     68
    .sgpr_spill_count: 0
    .symbol:         _Z11attn_kernelPKDF16_S0_S0_PDF16_PKjS3_.kd
    .uniform_work_group_size: 1
    .uses_dynamic_stack: false
    .vgpr_count:     248
    .vgpr_spill_count: 0
    .wavefront_size: 64
